# combine+LayerNorm2: weight/bias loads hoisted out of the token loop, per-group waits removed; token-top drain moved to the preload block
# speedup vs baseline: 1.0038x; 1.0034x over previous
; #define GAS __attribute__((address_space(1)))
; #define LAS __attribute__((address_space(3)))
; #define PHASE_ARGS() CArgsP ap = (CArgsP)__builtin_amdgcn_kernarg_segment_ptr(); asm volatile("" : "+s"(ap))
; #define PHASE_IDS() int tid = threadIdx.x; asm volatile("" : "+v"(tid)); const int lane = tid & 63, w = __builtin_amdgcn_readfirstlane(tid >> 6); (void)lane; (void)w
; template <bool Y8, bool LAST>
; __device__ __forceinline__ void combine_ln2_phase(Frame& F, int layer) {
;     PHASE_ARGS(); GAS float* OUT = (GAS float*)(GAS float*)ap->out;
;     const GAS bf16_t* Y = (const GAS bf16_t*)(F.ws + WS_Y); const GAS bf16_t* X1B = (const GAS bf16_t*)(F.ws + WS_X1B); GAS bf16_t* XB = (GAS bf16_t*)(F.ws + WS_XB); GAS unsigned char* XB8 = F.ws + WS_XB8;
;     const GAS float* g2 = GIN(18) + (size_t)layer * D_MODEL; const GAS float* b2 = GIN(19) + (size_t)layer * D_MODEL;
;     const GAS int* PE = (const GAS int*)(F.ws + WS_PE); const GAS int* PP = (const GAS int*)(F.ws + WS_PP); const GAS float* PG = (const GAS float*)(F.ws + WS_PG);
;     const LAS int* toff = (const LAS int*)(F.lds + LDS_TAB);
;     PHASE_IDS();
;     const int gw = F.bid * 8 + w, NGW = F.G * 8;
;     for (int tb = gw; tb < T; tb += 8 * NGW) {
;         int myrow = 0; float mygate = 0.f;
;         { const int tl = tb + (lane >> 3) * NGW; if (tl < T) { const int e = PE[(size_t)tl * 8 + (lane & 7)]; myrow = toff[e] * 256 + PP[(size_t)tl * 8 + (lane & 7)]; mygate = PG[(size_t)tl * 8 + (lane & 7)]; } }
;     ...
;         for (int j = 0; j < 4; ++j) { const int c = 8 * lane + 512 * j;
;             const f32x4 o0 = a[j][0] * rstd * *(const GAS f32x4*)(g2 + c) + *(const GAS f32x4*)(b2 + c), o1 = a[j][1] * rstd * *(const GAS f32x4*)(g2 + c + 4) + *(const GAS f32x4*)(b2 + c + 4);
.LBB0_2027:
	s_or_b64 exec, exec, s[4:5]
	v_readlane_b32 s8, v254, 1
	v_readlane_b32 s9, v254, 2
	s_waitcnt vmcnt(0)
	v_mov_b32_e32 v2, v0
	s_waitcnt lgkmcnt(0)
	s_barrier
	s_lshl_b32 s0, s0, 3
	v_readfirstlane_b32 s1, v2
	s_ashr_i32 s1, s1, 6
	s_add_i32 s0, s1, s0
	s_cmpk_gt_i32 s0, 0x3fff
	s_cbranch_scc1 .LBB0_2036
	s_load_dwordx4 s[4:7], s[8:9], 0x90
	s_add_u32 s8, s14, 0x35300000
	v_and_b32_e32 v3, 63, v2
	s_addc_u32 s9, s15, 0
	v_mov_b32_e32 v19, 0
	v_lshlrev_b32_e32 v18, 3, v3
	s_add_u32 s10, s14, 0x35400000
	v_lshl_add_u64 v[22:23], s[14:15], 0, v[18:19]
	v_lshlrev_b32_e32 v18, 4, v3
	s_addc_u32 s11, s15, 0
	v_lshl_add_u64 v[20:21], s[14:15], 0, v[18:19]
	v_lshlrev_b32_e32 v18, 5, v3
	v_mbcnt_lo_u32_b32 v3, -1, 0
	s_add_u32 s12, s14, 0x35500000
	s_waitcnt lgkmcnt(0)
	v_lshl_add_u64 v[8:9], s[4:5], 0, v[18:19]
	v_lshl_add_u64 v[10:11], s[6:7], 0, v[18:19]
	v_or_b32_e32 v14, 0x1000, v18
	v_mov_b32_e32 v15, v19
	v_or_b32_e32 v18, 0x1800, v18
	v_mbcnt_hi_u32_b32 v3, -1, v3
	s_addc_u32 s13, s15, 0
	s_mov_b64 s[14:15], 0x31300000
	v_lshl_add_u64 v[12:13], s[4:5], 0, v[14:15]
	v_lshl_add_u64 v[16:17], s[4:5], 0, v[18:19]
	s_mov_b64 s[4:5], 0x2d300000
	v_lshlrev_b32_e32 v24, 2, v3
	s_lshl_b32 s2, s16, 3
	v_bfe_u32 v1, v2, 3, 3
	s_mov_b64 s[18:19], 0x3fb00000
	v_lshl_add_u64 v[6:7], v[20:21], 0, s[14:15]
	v_lshl_add_u64 v[20:21], v[20:21], 0, s[4:5]
	s_mov_b64 s[4:5], 0x6ff00000
	v_and_b32_e32 v56, 0x100, v24
	v_and_b32_e32 v24, 64, v3
	s_add_i32 s1, s3, 0x24000
	v_mul_lo_u32 v1, v1, s2
	v_and_b32_e32 v2, 7, v2
	v_lshl_add_u64 v[4:5], v[22:23], 0, s[18:19]
	s_add_i32 s3, s3, 0x24100
	s_lshl_b32 s18, s16, 6
	v_lshl_add_u64 v[14:15], s[6:7], 0, v[14:15]
	v_lshl_add_u64 v[18:19], s[6:7], 0, v[18:19]
	v_lshl_add_u64 v[22:23], v[22:23], 0, s[4:5]
	s_movk_i32 s5, 0x4000
	s_mov_b32 s4, 0x3fb504f3
	v_add_u32_e32 v57, 64, v24
	v_xor_b32_e32 v58, 1, v3
	v_xor_b32_e32 v59, 2, v3
	v_xor_b32_e32 v60, 4, v3
	v_xor_b32_e32 v61, 8, v3
	v_xor_b32_e32 v62, 16, v3
	v_xor_b32_e32 v63, 32, v3
	v_mov_b32_e32 v64, 0x3727c5ac
	s_mov_b32 s19, 0x800000
	global_load_dwordx4 v[128:131], v[8:9], off offset:16
	global_load_dwordx4 v[132:135], v[8:9], off
	global_load_dwordx4 v[136:139], v[10:11], off offset:16
	global_load_dwordx4 v[140:143], v[10:11], off
	global_load_dwordx4 v[144:147], v[10:11], off offset:2048
	global_load_dwordx4 v[148:151], v[8:9], off offset:2048
	global_load_dwordx4 v[152:155], v[8:9], off offset:2064
	global_load_dwordx4 v[156:159], v[10:11], off offset:2064
	global_load_dwordx4 v[160:163], v[14:15], off
	global_load_dwordx4 v[164:167], v[12:13], off
	global_load_dwordx4 v[168:171], v[12:13], off offset:16
	global_load_dwordx4 v[172:175], v[14:15], off offset:16
	global_load_dwordx4 v[176:179], v[18:19], off
	global_load_dwordx4 v[180:183], v[16:17], off
	global_load_dwordx4 v[184:187], v[16:17], off offset:16
	global_load_dwordx4 v[188:191], v[18:19], off offset:16
	s_waitcnt vmcnt(0)
	s_branch .LBB0_2030

; template <bool Y8, bool LAST>
; __device__ __forceinline__ void combine_ln2_phase(Frame& F, int layer) {
;     ...
;     for (int tb = gw; tb < T; tb += 8 * NGW) {
;         int myrow = 0; float mygate = 0.f;
;         { const int tl = tb + (lane >> 3) * NGW; if (tl < T) { const int e = PE[(size_t)tl * 8 + (lane & 7)]; myrow = toff[e] * 256 + PP[(size_t)tl * 8 + (lane & 7)]; mygate = PG[(size_t)tl * 8 + (lane & 7)]; } }
.LBB0_2030:
	v_add_u32_e32 v24, s0, v1
	v_cmp_gt_i32_e32 vcc, s5, v24
	s_waitcnt vmcnt(0)
	v_mov_b32_e32 v65, 0
	v_mov_b32_e32 v66, 0
	s_and_saveexec_b64 s[6:7], vcc
	s_cbranch_execz .LBB0_2032
	v_ashrrev_i32_e32 v25, 31, v24
	v_lshlrev_b64 v[24:25], 5, v[24:25]
	v_lshl_or_b32 v24, v2, 2, v24
	v_lshl_add_u64 v[26:27], s[8:9], 0, v[24:25]
	global_load_dword v28, v[26:27], off
	v_lshl_add_u64 v[26:27], s[10:11], 0, v[24:25]
	v_lshl_add_u64 v[24:25], s[12:13], 0, v[24:25]
	global_load_dword v29, v[26:27], off
	global_load_dword v65, v[24:25], off
	s_waitcnt vmcnt(2)
	v_lshl_add_u32 v24, v28, 2, s1
	ds_read_b32 v24, v24
	s_waitcnt vmcnt(0) lgkmcnt(0)
	v_lshl_add_u32 v66, v24, 8, v29

; #define GAS __attribute__((address_space(1)))
; template <bool Y8, bool LAST>
; __device__ __forceinline__ void combine_ln2_phase(Frame& F, int layer) {
;     ...
;       for (int tj = 0; tj < 8; ++tj) { const int t = tb + tj * NGW; if (t >= T) break;
;         f32x4 a[4][2];
; #pragma unroll
;         for (int j = 0; j < 4; ++j) { a[j][0] = (f32x4){0.f, 0.f, 0.f, 0.f}; a[j][1] = (f32x4){0.f, 0.f, 0.f, 0.f}; }
; #pragma unroll
;         for (int k = 0; k < 9; ++k) { size_t row; float gt;
;             if (k < 8) { row = (size_t)__shfl(myrow, tj * 8 + k); gt = __shfl(mygate, tj * 8 + k); }
;             else { row = (size_t)toff[N_EXPERTS] * 256 + t; gt = 1.0f; }
;             if constexpr (Y8) {
;                 const GAS u32x2* yp = (const GAS u32x2*)((const GAS unsigned char*)Y + row * D_MODEL) + lane;
; #pragma unroll
;                 for (int j = 0; j < 4; ++j) { const u32x2 y = yp[64 * j];
;                     const f32x2 p0 = __builtin_amdgcn_cvt_pk_f32_fp8((int)y.x, false), p1 = __builtin_amdgcn_cvt_pk_f32_fp8((int)y.x, true), p2 = __builtin_amdgcn_cvt_pk_f32_fp8((int)y.y, false), p3 = __builtin_amdgcn_cvt_pk_f32_fp8((int)y.y, true);
;                     a[j][0] += (f32x4){p0[0], p0[1], p1[0], p1[1]} * gt; a[j][1] += (f32x4){p2[0], p2[1], p3[0], p3[1]} * gt; }
;             } else {
;             const GAS u32x4* yp = (const GAS u32x4*)(Y + row * D_MODEL) + lane;
; #pragma unroll
;             for (int j = 0; j < 4; ++j) { const u32x4 y = yp[64 * j];
;                 a[j][0] += (f32x4){bflo(y.x), bfhi(y.x), bflo(y.y), bfhi(y.y)} * gt; a[j][1] += (f32x4){bflo(y.z), bfhi(y.z), bflo(y.w), bfhi(y.w)} * gt; } } }
.LBB0_2034:
	s_cmpk_gt_i32 s6, 0x3fff
	s_mov_b64 s[14:15], -1
	s_cbranch_scc1 .LBB0_2033
	v_or_b32_e32 v24, s20, v56
	ds_bpermute_b32 v26, v24, v66
	ds_bpermute_b32 v32, v24, v66 offset:4
	ds_bpermute_b32 v44, v24, v66 offset:12
	ds_bpermute_b32 v46, v24, v65
	ds_bpermute_b32 v48, v24, v65 offset:4
	s_waitcnt lgkmcnt(4)
	v_ashrrev_i32_e32 v27, 31, v26
	v_lshlrev_b64 v[26:27], 11, v[26:27]
	v_lshl_add_u64 v[26:27], v[4:5], 0, v[26:27]
	s_waitcnt lgkmcnt(3)
	v_ashrrev_i32_e32 v33, 31, v32
	global_load_dwordx2 v[28:29], v[26:27], off
	global_load_dwordx2 v[30:31], v[26:27], off offset:512
	global_load_dwordx2 v[34:35], v[26:27], off offset:1024
	global_load_dwordx2 v[36:37], v[26:27], off offset:1536
	v_lshlrev_b64 v[26:27], 11, v[32:33]
	v_lshl_add_u64 v[26:27], v[4:5], 0, v[26:27]
	global_load_dwordx2 v[32:33], v[26:27], off
	global_load_dwordx2 v[38:39], v[26:27], off offset:512
	global_load_dwordx2 v[40:41], v[26:27], off offset:1024
	global_load_dwordx2 v[42:43], v[26:27], off offset:1536
	ds_bpermute_b32 v26, v24, v66 offset:8
	s_waitcnt lgkmcnt(3)
	v_ashrrev_i32_e32 v45, 31, v44
	v_lshlrev_b64 v[44:45], 11, v[44:45]
	v_lshl_add_u64 v[44:45], v[4:5], 0, v[44:45]
	v_mov_b32_e32 v25, s3
	s_waitcnt lgkmcnt(0)
	v_ashrrev_i32_e32 v27, 31, v26
	v_lshlrev_b64 v[26:27], 11, v[26:27]
	v_lshl_add_u64 v[26:27], v[4:5], 0, v[26:27]
	global_load_dwordx2 v[50:51], v[26:27], off
	global_load_dwordx2 v[52:53], v[26:27], off offset:512
	global_load_dwordx2 v[54:55], v[26:27], off offset:1024
	global_load_dwordx2 v[68:69], v[26:27], off offset:1536
	global_load_dwordx2 v[70:71], v[44:45], off
	global_load_dwordx2 v[72:73], v[44:45], off offset:512
	global_load_dwordx2 v[74:75], v[44:45], off offset:1024
	global_load_dwordx2 v[76:77], v[44:45], off offset:1536
	s_ashr_i32 s7, s6, 31
	s_lshl_b64 s[14:15], s[6:7], 11
	v_or_b32_e32 v67, 28, v24
	s_lshl_b64 s[16:17], s[6:7], 12
	v_cmp_lt_i32_e32 vcc, v58, v57
	s_add_i32 s20, s20, 32
	s_add_i32 s6, s6, s2
	s_cmpk_eq_i32 s20, 0x100
	s_waitcnt vmcnt(15)
	v_cvt_pk_f32_fp8_e32 v[26:27], v28
	s_waitcnt vmcnt(14)
	v_cvt_pk_f32_fp8_e32 v[80:81], v30
	v_cvt_pk_f32_fp8_sdwa v[82:83], v30 src0_sel:WORD_1
	v_cvt_pk_f32_fp8_e32 v[84:85], v31
	v_cvt_pk_f32_fp8_sdwa v[30:31], v31 src0_sel:WORD_1
	s_waitcnt vmcnt(10)
	v_cvt_pk_f32_fp8_e32 v[104:105], v38
	v_cvt_pk_f32_fp8_sdwa v[106:107], v38 src0_sel:WORD_1
	v_cvt_pk_f32_fp8_e32 v[108:109], v39
	v_cvt_pk_f32_fp8_sdwa v[38:39], v39 src0_sel:WORD_1
	v_cvt_pk_f32_fp8_sdwa v[44:45], v28 src0_sel:WORD_1
	v_cvt_pk_f32_fp8_e32 v[78:79], v29
	v_cvt_pk_f32_fp8_sdwa v[28:29], v29 src0_sel:WORD_1
	v_cvt_pk_f32_fp8_e32 v[86:87], v34
	v_cvt_pk_f32_fp8_sdwa v[88:89], v34 src0_sel:WORD_1
	v_cvt_pk_f32_fp8_e32 v[90:91], v35
	v_cvt_pk_f32_fp8_sdwa v[34:35], v35 src0_sel:WORD_1
	v_cvt_pk_f32_fp8_e32 v[92:93], v36
	v_cvt_pk_f32_fp8_sdwa v[94:95], v36 src0_sel:WORD_1
	v_cvt_pk_f32_fp8_e32 v[96:97], v37
	v_cvt_pk_f32_fp8_sdwa v[36:37], v37 src0_sel:WORD_1
	v_pk_fma_f32 v[84:85], v[46:47], v[84:85], 0 op_sel_hi:[0,1,0]
	v_pk_fma_f32 v[30:31], v[46:47], v[30:31], 0 op_sel_hi:[0,1,0]
	v_cvt_pk_f32_fp8_e32 v[98:99], v32
	v_cvt_pk_f32_fp8_sdwa v[100:101], v32 src0_sel:WORD_1
	v_cvt_pk_f32_fp8_e32 v[102:103], v33
	v_cvt_pk_f32_fp8_sdwa v[32:33], v33 src0_sel:WORD_1
	s_waitcnt vmcnt(9)
	v_cvt_pk_f32_fp8_e32 v[110:111], v40
	v_cvt_pk_f32_fp8_sdwa v[112:113], v40 src0_sel:WORD_1
	v_cvt_pk_f32_fp8_e32 v[114:115], v41
	v_cvt_pk_f32_fp8_sdwa v[40:41], v41 src0_sel:WORD_1
	s_waitcnt vmcnt(8)
	v_cvt_pk_f32_fp8_e32 v[116:117], v42
	v_cvt_pk_f32_fp8_sdwa v[118:119], v42 src0_sel:WORD_1
	v_cvt_pk_f32_fp8_sdwa v[120:121], v43 src0_sel:WORD_1
	v_pk_fma_f32 v[30:31], v[48:49], v[38:39], v[30:31] op_sel_hi:[0,1,1]
	v_pk_fma_f32 v[38:39], v[48:49], v[108:109], v[84:85] op_sel_hi:[0,1,1]
	v_cvt_pk_f32_fp8_e32 v[84:85], v43
	v_pk_fma_f32 v[26:27], v[46:47], v[26:27], 0 op_sel_hi:[0,1,0]
	v_pk_fma_f32 v[44:45], v[46:47], v[44:45], 0 op_sel_hi:[0,1,0]
	v_pk_fma_f32 v[78:79], v[46:47], v[78:79], 0 op_sel_hi:[0,1,0]
	v_pk_fma_f32 v[28:29], v[46:47], v[28:29], 0 op_sel_hi:[0,1,0]
	v_pk_fma_f32 v[80:81], v[46:47], v[80:81], 0 op_sel_hi:[0,1,0]
	v_pk_fma_f32 v[82:83], v[46:47], v[82:83], 0 op_sel_hi:[0,1,0]
	v_pk_fma_f32 v[86:87], v[46:47], v[86:87], 0 op_sel_hi:[0,1,0]
	v_pk_fma_f32 v[88:89], v[46:47], v[88:89], 0 op_sel_hi:[0,1,0]
	v_pk_fma_f32 v[90:91], v[46:47], v[90:91], 0 op_sel_hi:[0,1,0]
	v_pk_fma_f32 v[34:35], v[46:47], v[34:35], 0 op_sel_hi:[0,1,0]
	v_pk_fma_f32 v[92:93], v[46:47], v[92:93], 0 op_sel_hi:[0,1,0]
	v_pk_fma_f32 v[94:95], v[46:47], v[94:95], 0 op_sel_hi:[0,1,0]
	v_pk_fma_f32 v[96:97], v[46:47], v[96:97], 0 op_sel_hi:[0,1,0]
	v_pk_fma_f32 v[36:37], v[46:47], v[36:37], 0 op_sel_hi:[0,1,0]
	v_pk_fma_f32 v[44:45], v[48:49], v[100:101], v[44:45] op_sel_hi:[0,1,1]
	v_pk_fma_f32 v[26:27], v[48:49], v[98:99], v[26:27] op_sel_hi:[0,1,1]
	v_pk_fma_f32 v[28:29], v[48:49], v[32:33], v[28:29] op_sel_hi:[0,1,1]
	v_pk_fma_f32 v[32:33], v[48:49], v[102:103], v[78:79] op_sel_hi:[0,1,1]
	v_pk_fma_f32 v[46:47], v[48:49], v[106:107], v[82:83] op_sel_hi:[0,1,1]
	v_pk_fma_f32 v[78:79], v[48:49], v[104:105], v[80:81] op_sel_hi:[0,1,1]
	v_pk_fma_f32 v[80:81], v[48:49], v[112:113], v[88:89] op_sel_hi:[0,1,1]
	v_pk_fma_f32 v[82:83], v[48:49], v[110:111], v[86:87] op_sel_hi:[0,1,1]
	v_pk_fma_f32 v[34:35], v[48:49], v[40:41], v[34:35] op_sel_hi:[0,1,1]
	v_pk_fma_f32 v[40:41], v[48:49], v[114:115], v[90:91] op_sel_hi:[0,1,1]
	v_pk_fma_f32 v[86:87], v[48:49], v[118:119], v[94:95] op_sel_hi:[0,1,1]
	v_pk_fma_f32 v[88:89], v[48:49], v[116:117], v[92:93] op_sel_hi:[0,1,1]
	v_pk_fma_f32 v[36:37], v[48:49], v[120:121], v[36:37] op_sel_hi:[0,1,1]
	v_pk_fma_f32 v[48:49], v[48:49], v[84:85], v[96:97] op_sel_hi:[0,1,1]
	ds_bpermute_b32 v84, v24, v65 offset:8
	s_waitcnt vmcnt(7)
; #define GAS __attribute__((address_space(1)))
; template <bool Y8, bool LAST>
; __device__ __forceinline__ void combine_ln2_phase(Frame& F, int layer) {
;     ...
;         for (int k = 0; k < 9; ++k) { size_t row; float gt;
;             if (k < 8) { row = (size_t)__shfl(myrow, tj * 8 + k); gt = __shfl(mygate, tj * 8 + k); }
;             else { row = (size_t)toff[N_EXPERTS] * 256 + t; gt = 1.0f; }
;             if constexpr (Y8) {
;                 const GAS u32x2* yp = (const GAS u32x2*)((const GAS unsigned char*)Y + row * D_MODEL) + lane;
; #pragma unroll
;                 for (int j = 0; j < 4; ++j) { const u32x2 y = yp[64 * j];
;                     const f32x2 p0 = __builtin_amdgcn_cvt_pk_f32_fp8((int)y.x, false), p1 = __builtin_amdgcn_cvt_pk_f32_fp8((int)y.x, true), p2 = __builtin_amdgcn_cvt_pk_f32_fp8((int)y.y, false), p3 = __builtin_amdgcn_cvt_pk_f32_fp8((int)y.y, true);
;                     a[j][0] += (f32x4){p0[0], p0[1], p1[0], p1[1]} * gt; a[j][1] += (f32x4){p2[0], p2[1], p3[0], p3[1]} * gt; }
;             } else {
;             const GAS u32x4* yp = (const GAS u32x4*)(Y + row * D_MODEL) + lane;
; #pragma unroll
;             for (int j = 0; j < 4; ++j) { const u32x4 y = yp[64 * j];
;                 a[j][0] += (f32x4){bflo(y.x), bfhi(y.x), bflo(y.y), bfhi(y.y)} * gt; a[j][1] += (f32x4){bflo(y.z), bfhi(y.z), bflo(y.w), bfhi(y.w)} * gt; } } }
	v_cvt_pk_f32_fp8_e32 v[92:93], v50
	v_cvt_pk_f32_fp8_sdwa v[94:95], v50 src0_sel:WORD_1
	v_cvt_pk_f32_fp8_e32 v[96:97], v51
	v_cvt_pk_f32_fp8_sdwa v[50:51], v51 src0_sel:WORD_1
	ds_bpermute_b32 v42, v24, v66 offset:16
	s_waitcnt lgkmcnt(1)
	v_pk_fma_f32 v[26:27], v[84:85], v[92:93], v[26:27] op_sel_hi:[0,1,1]
	v_pk_fma_f32 v[32:33], v[84:85], v[96:97], v[32:33] op_sel_hi:[0,1,1]
	v_pk_fma_f32 v[28:29], v[84:85], v[50:51], v[28:29] op_sel_hi:[0,1,1]
	s_waitcnt vmcnt(6)
	v_cvt_pk_f32_fp8_e32 v[50:51], v52
	v_cvt_pk_f32_fp8_sdwa v[92:93], v52 src0_sel:WORD_1
	v_cvt_pk_f32_fp8_e32 v[96:97], v53
	v_cvt_pk_f32_fp8_sdwa v[52:53], v53 src0_sel:WORD_1
	v_pk_fma_f32 v[50:51], v[84:85], v[50:51], v[78:79] op_sel_hi:[0,1,1]
	s_waitcnt vmcnt(5)
	v_cvt_pk_f32_fp8_sdwa v[78:79], v54 src0_sel:WORD_1
	v_pk_fma_f32 v[38:39], v[84:85], v[96:97], v[38:39] op_sel_hi:[0,1,1]
	v_pk_fma_f32 v[30:31], v[84:85], v[52:53], v[30:31] op_sel_hi:[0,1,1]
	v_cvt_pk_f32_fp8_e32 v[52:53], v54
	v_cvt_pk_f32_fp8_e32 v[96:97], v55
	v_cvt_pk_f32_fp8_sdwa v[54:55], v55 src0_sel:WORD_1
	s_waitcnt lgkmcnt(0)
	v_ashrrev_i32_e32 v43, 31, v42
	v_lshlrev_b64 v[42:43], 11, v[42:43]
	v_lshl_add_u64 v[42:43], v[4:5], 0, v[42:43]
	global_load_dwordx2 v[90:91], v[42:43], off
	v_pk_fma_f32 v[34:35], v[84:85], v[54:55], v[34:35] op_sel_hi:[0,1,1]
	s_waitcnt vmcnt(5)
	v_cvt_pk_f32_fp8_e32 v[54:55], v68
	v_pk_fma_f32 v[44:45], v[84:85], v[94:95], v[44:45] op_sel_hi:[0,1,1]
	global_load_dwordx2 v[94:95], v[42:43], off offset:512
	v_pk_fma_f32 v[52:53], v[84:85], v[52:53], v[82:83] op_sel_hi:[0,1,1]
	v_pk_fma_f32 v[54:55], v[84:85], v[54:55], v[88:89] op_sel_hi:[0,1,1]
	ds_bpermute_b32 v88, v24, v66 offset:20
	v_cvt_pk_f32_fp8_e32 v[82:83], v69
	v_pk_fma_f32 v[46:47], v[84:85], v[92:93], v[46:47] op_sel_hi:[0,1,1]
	global_load_dwordx2 v[92:93], v[42:43], off offset:1024
	v_pk_fma_f32 v[78:79], v[84:85], v[78:79], v[80:81] op_sel_hi:[0,1,1]
	v_cvt_pk_f32_fp8_sdwa v[80:81], v68 src0_sel:WORD_1
	v_cvt_pk_f32_fp8_sdwa v[68:69], v69 src0_sel:WORD_1
	s_waitcnt lgkmcnt(0)
	v_ashrrev_i32_e32 v89, 31, v88
	v_pk_fma_f32 v[48:49], v[84:85], v[82:83], v[48:49] op_sel_hi:[0,1,1]
	v_lshlrev_b64 v[82:83], 11, v[88:89]
	v_lshl_add_u64 v[82:83], v[4:5], 0, v[82:83]
	v_pk_fma_f32 v[40:41], v[84:85], v[96:97], v[40:41] op_sel_hi:[0,1,1]
	v_pk_fma_f32 v[80:81], v[84:85], v[80:81], v[86:87] op_sel_hi:[0,1,1]
	v_pk_fma_f32 v[36:37], v[84:85], v[68:69], v[36:37] op_sel_hi:[0,1,1]
	global_load_dwordx2 v[84:85], v[82:83], off
	ds_bpermute_b32 v68, v24, v65 offset:12
	global_load_dwordx2 v[42:43], v[42:43], off offset:1536
	s_waitcnt vmcnt(8)
	v_cvt_pk_f32_fp8_e32 v[88:89], v70
	v_cvt_pk_f32_fp8_sdwa v[96:97], v71 src0_sel:WORD_1
	v_cvt_pk_f32_fp8_sdwa v[86:87], v70 src0_sel:WORD_1
	v_cvt_pk_f32_fp8_e32 v[70:71], v71
	s_waitcnt lgkmcnt(0)
	v_pk_fma_f32 v[26:27], v[68:69], v[88:89], v[26:27] op_sel_hi:[0,1,1]
	v_pk_fma_f32 v[28:29], v[68:69], v[96:97], v[28:29] op_sel_hi:[0,1,1]
	s_waitcnt vmcnt(7)
	v_cvt_pk_f32_fp8_sdwa v[88:89], v73 src0_sel:WORD_1
	global_load_dwordx2 v[96:97], v[82:83], off offset:512
	v_pk_fma_f32 v[44:45], v[68:69], v[86:87], v[44:45] op_sel_hi:[0,1,1]
	v_pk_fma_f32 v[32:33], v[68:69], v[70:71], v[32:33] op_sel_hi:[0,1,1]
	v_cvt_pk_f32_fp8_e32 v[70:71], v72
	v_cvt_pk_f32_fp8_sdwa v[86:87], v72 src0_sel:WORD_1
	v_cvt_pk_f32_fp8_e32 v[72:73], v73
	v_pk_fma_f32 v[30:31], v[68:69], v[88:89], v[30:31] op_sel_hi:[0,1,1]
	global_load_dwordx2 v[88:89], v[82:83], off offset:1024
	v_pk_fma_f32 v[46:47], v[68:69], v[86:87], v[46:47] op_sel_hi:[0,1,1]
	v_pk_fma_f32 v[50:51], v[68:69], v[70:71], v[50:51] op_sel_hi:[0,1,1]
	v_pk_fma_f32 v[38:39], v[68:69], v[72:73], v[38:39] op_sel_hi:[0,1,1]
	s_waitcnt vmcnt(8)
	v_cvt_pk_f32_fp8_e32 v[70:71], v74
	v_cvt_pk_f32_fp8_sdwa v[72:73], v74 src0_sel:WORD_1
	v_cvt_pk_f32_fp8_sdwa v[86:87], v75 src0_sel:WORD_1
	v_cvt_pk_f32_fp8_e32 v[74:75], v75
	v_pk_fma_f32 v[52:53], v[68:69], v[70:71], v[52:53] op_sel_hi:[0,1,1]
	v_pk_fma_f32 v[72:73], v[68:69], v[72:73], v[78:79] op_sel_hi:[0,1,1]
	s_waitcnt vmcnt(7)
	v_cvt_pk_f32_fp8_sdwa v[70:71], v76 src0_sel:WORD_1
	v_pk_fma_f32 v[40:41], v[68:69], v[74:75], v[40:41] op_sel_hi:[0,1,1]
	v_cvt_pk_f32_fp8_e32 v[74:75], v76
	v_cvt_pk_f32_fp8_e32 v[78:79], v77
	v_cvt_pk_f32_fp8_sdwa v[76:77], v77 src0_sel:WORD_1
	v_pk_fma_f32 v[34:35], v[68:69], v[86:87], v[34:35] op_sel_hi:[0,1,1]
	v_pk_fma_f32 v[54:55], v[68:69], v[74:75], v[54:55] op_sel_hi:[0,1,1]
	global_load_dwordx2 v[74:75], v[82:83], off offset:1536
	ds_bpermute_b32 v82, v24, v66 offset:24
	v_pk_fma_f32 v[70:71], v[68:69], v[70:71], v[80:81] op_sel_hi:[0,1,1]
	v_pk_fma_f32 v[36:37], v[68:69], v[76:77], v[36:37] op_sel_hi:[0,1,1]
	v_pk_fma_f32 v[48:49], v[68:69], v[78:79], v[48:49] op_sel_hi:[0,1,1]
	ds_bpermute_b32 v68, v24, v65 offset:16
	s_waitcnt lgkmcnt(1)
	v_ashrrev_i32_e32 v83, 31, v82
	s_waitcnt vmcnt(7)
	v_cvt_pk_f32_fp8_e32 v[76:77], v90
	v_cvt_pk_f32_fp8_sdwa v[86:87], v91 src0_sel:WORD_1
	v_cvt_pk_f32_fp8_sdwa v[78:79], v90 src0_sel:WORD_1
	v_cvt_pk_f32_fp8_e32 v[80:81], v91
	s_waitcnt lgkmcnt(0)
	v_pk_fma_f32 v[26:27], v[68:69], v[76:77], v[26:27] op_sel_hi:[0,1,1]
	v_lshlrev_b64 v[76:77], 11, v[82:83]
	v_pk_fma_f32 v[28:29], v[68:69], v[86:87], v[28:29] op_sel_hi:[0,1,1]
	s_waitcnt vmcnt(6)
	v_cvt_pk_f32_fp8_sdwa v[82:83], v94 src0_sel:WORD_1
	v_cvt_pk_f32_fp8_e32 v[86:87], v95
	v_cvt_pk_f32_fp8_sdwa v[90:91], v95 src0_sel:WORD_1
	v_pk_fma_f32 v[32:33], v[68:69], v[80:81], v[32:33] op_sel_hi:[0,1,1]
	v_cvt_pk_f32_fp8_e32 v[80:81], v94
	v_pk_fma_f32 v[46:47], v[68:69], v[82:83], v[46:47] op_sel_hi:[0,1,1]
	v_pk_fma_f32 v[38:39], v[68:69], v[86:87], v[38:39] op_sel_hi:[0,1,1]
	v_pk_fma_f32 v[30:31], v[68:69], v[90:91], v[30:31] op_sel_hi:[0,1,1]
	s_waitcnt vmcnt(5)
; #define GAS __attribute__((address_space(1)))
; template <bool Y8, bool LAST>
; __device__ __forceinline__ void combine_ln2_phase(Frame& F, int layer) {
;     ...
;         for (int k = 0; k < 9; ++k) { size_t row; float gt;
;             if (k < 8) { row = (size_t)__shfl(myrow, tj * 8 + k); gt = __shfl(mygate, tj * 8 + k); }
;             else { row = (size_t)toff[N_EXPERTS] * 256 + t; gt = 1.0f; }
;             if constexpr (Y8) {
;                 const GAS u32x2* yp = (const GAS u32x2*)((const GAS unsigned char*)Y + row * D_MODEL) + lane;
; #pragma unroll
;                 for (int j = 0; j < 4; ++j) { const u32x2 y = yp[64 * j];
;                     const f32x2 p0 = __builtin_amdgcn_cvt_pk_f32_fp8((int)y.x, false), p1 = __builtin_amdgcn_cvt_pk_f32_fp8((int)y.x, true), p2 = __builtin_amdgcn_cvt_pk_f32_fp8((int)y.y, false), p3 = __builtin_amdgcn_cvt_pk_f32_fp8((int)y.y, true);
;                     a[j][0] += (f32x4){p0[0], p0[1], p1[0], p1[1]} * gt; a[j][1] += (f32x4){p2[0], p2[1], p3[0], p3[1]} * gt; }
;             } else {
;             const GAS u32x4* yp = (const GAS u32x4*)(Y + row * D_MODEL) + lane;
; #pragma unroll
;             for (int j = 0; j < 4; ++j) { const u32x4 y = yp[64 * j];
;                 a[j][0] += (f32x4){bflo(y.x), bfhi(y.x), bflo(y.y), bfhi(y.y)} * gt; a[j][1] += (f32x4){bflo(y.z), bfhi(y.z), bflo(y.w), bfhi(y.w)} * gt; } } }
	v_cvt_pk_f32_fp8_e32 v[82:83], v92
	v_cvt_pk_f32_fp8_sdwa v[86:87], v92 src0_sel:WORD_1
	v_cvt_pk_f32_fp8_e32 v[90:91], v93
	v_cvt_pk_f32_fp8_sdwa v[92:93], v93 src0_sel:WORD_1
	v_lshl_add_u64 v[76:77], v[4:5], 0, v[76:77]
	v_pk_fma_f32 v[44:45], v[68:69], v[78:79], v[44:45] op_sel_hi:[0,1,1]
	global_load_dwordx2 v[78:79], v[76:77], off
	v_pk_fma_f32 v[50:51], v[68:69], v[80:81], v[50:51] op_sel_hi:[0,1,1]
	global_load_dwordx2 v[80:81], v[76:77], off offset:512
	v_pk_fma_f32 v[52:53], v[68:69], v[82:83], v[52:53] op_sel_hi:[0,1,1]
	v_pk_fma_f32 v[72:73], v[68:69], v[86:87], v[72:73] op_sel_hi:[0,1,1]
	v_pk_fma_f32 v[40:41], v[68:69], v[90:91], v[40:41] op_sel_hi:[0,1,1]
	v_pk_fma_f32 v[34:35], v[68:69], v[92:93], v[34:35] op_sel_hi:[0,1,1]
	global_load_dwordx2 v[82:83], v[76:77], off offset:1024
	s_waitcnt vmcnt(6)
	v_cvt_pk_f32_fp8_e32 v[86:87], v42
	v_cvt_pk_f32_fp8_sdwa v[90:91], v42 src0_sel:WORD_1
	v_cvt_pk_f32_fp8_e32 v[92:93], v43
	v_cvt_pk_f32_fp8_sdwa v[42:43], v43 src0_sel:WORD_1
	v_pk_fma_f32 v[54:55], v[68:69], v[86:87], v[54:55] op_sel_hi:[0,1,1]
	v_pk_fma_f32 v[70:71], v[68:69], v[90:91], v[70:71] op_sel_hi:[0,1,1]
	v_pk_fma_f32 v[48:49], v[68:69], v[92:93], v[48:49] op_sel_hi:[0,1,1]
	v_pk_fma_f32 v[36:37], v[68:69], v[42:43], v[36:37] op_sel_hi:[0,1,1]
	ds_bpermute_b32 v42, v24, v65 offset:20
	v_cvt_pk_f32_fp8_e32 v[86:87], v84
	v_cvt_pk_f32_fp8_sdwa v[90:91], v84 src0_sel:WORD_1
	v_cvt_pk_f32_fp8_e32 v[92:93], v85
	v_cvt_pk_f32_fp8_sdwa v[84:85], v85 src0_sel:WORD_1
	s_waitcnt lgkmcnt(0)
	v_pk_fma_f32 v[26:27], v[42:43], v[86:87], v[26:27] op_sel_hi:[0,1,1]
	v_pk_fma_f32 v[44:45], v[42:43], v[90:91], v[44:45] op_sel_hi:[0,1,1]
	s_waitcnt vmcnt(5)
	v_cvt_pk_f32_fp8_sdwa v[86:87], v96 src0_sel:WORD_1
	v_pk_fma_f32 v[28:29], v[42:43], v[84:85], v[28:29] op_sel_hi:[0,1,1]
	v_cvt_pk_f32_fp8_e32 v[84:85], v96
	v_cvt_pk_f32_fp8_sdwa v[90:91], v97 src0_sel:WORD_1
	v_pk_fma_f32 v[46:47], v[42:43], v[86:87], v[46:47] op_sel_hi:[0,1,1]
	s_waitcnt vmcnt(4)
	v_cvt_pk_f32_fp8_sdwa v[86:87], v88 src0_sel:WORD_1
	v_pk_fma_f32 v[50:51], v[42:43], v[84:85], v[50:51] op_sel_hi:[0,1,1]
	v_cvt_pk_f32_fp8_e32 v[84:85], v88
	v_pk_fma_f32 v[30:31], v[42:43], v[90:91], v[30:31] op_sel_hi:[0,1,1]
	v_cvt_pk_f32_fp8_sdwa v[90:91], v89 src0_sel:WORD_1
	v_cvt_pk_f32_fp8_e32 v[88:89], v89
	v_pk_fma_f32 v[52:53], v[42:43], v[84:85], v[52:53] op_sel_hi:[0,1,1]
	ds_read_b32 v84, v25
	v_cvt_pk_f32_fp8_e32 v[96:97], v97
	v_pk_fma_f32 v[72:73], v[42:43], v[86:87], v[72:73] op_sel_hi:[0,1,1]
	v_pk_fma_f32 v[40:41], v[42:43], v[88:89], v[40:41] op_sel_hi:[0,1,1]
	s_waitcnt vmcnt(3)
	v_cvt_pk_f32_fp8_e32 v[86:87], v74
	v_cvt_pk_f32_fp8_sdwa v[88:89], v74 src0_sel:WORD_1
	s_waitcnt lgkmcnt(0)
	v_ashrrev_i32_e32 v85, 31, v84
	v_cvt_pk_f32_fp8_sdwa v[98:99], v75 src0_sel:WORD_1
	v_cvt_pk_f32_fp8_e32 v[74:75], v75
	v_lshlrev_b64 v[84:85], 19, v[84:85]
	v_lshl_add_u64 v[84:85], v[4:5], 0, v[84:85]
	v_lshl_add_u64 v[84:85], v[84:85], 0, s[14:15]
	global_load_dwordx2 v[68:69], v[76:77], off offset:1536
	v_pk_fma_f32 v[32:33], v[42:43], v[92:93], v[32:33] op_sel_hi:[0,1,1]
	v_pk_fma_f32 v[38:39], v[42:43], v[96:97], v[38:39] op_sel_hi:[0,1,1]
	v_pk_fma_f32 v[34:35], v[42:43], v[90:91], v[34:35] op_sel_hi:[0,1,1]
	v_pk_fma_f32 v[70:71], v[42:43], v[88:89], v[70:71] op_sel_hi:[0,1,1]
	v_pk_fma_f32 v[54:55], v[42:43], v[86:87], v[54:55] op_sel_hi:[0,1,1]
	v_pk_fma_f32 v[36:37], v[42:43], v[98:99], v[36:37] op_sel_hi:[0,1,1]
	v_pk_fma_f32 v[42:43], v[42:43], v[74:75], v[48:49] op_sel_hi:[0,1,1]
	global_load_dwordx2 v[74:75], v[84:85], off offset:512
	ds_bpermute_b32 v76, v67, v66
	global_load_dwordx2 v[90:91], v[84:85], off
	ds_bpermute_b32 v48, v24, v65 offset:24
	s_waitcnt lgkmcnt(1)
	v_ashrrev_i32_e32 v77, 31, v76
	v_lshlrev_b64 v[76:77], 11, v[76:77]
	v_lshl_add_u64 v[76:77], v[4:5], 0, v[76:77]
	global_load_dwordx2 v[94:95], v[76:77], off
	global_load_dwordx2 v[92:93], v[76:77], off offset:512
	global_load_dwordx2 v[96:97], v[76:77], off offset:1024
	s_waitcnt vmcnt(8)
	v_cvt_pk_f32_fp8_e32 v[24:25], v78
	global_load_dwordx2 v[76:77], v[76:77], off offset:1536
	v_cvt_pk_f32_fp8_sdwa v[86:87], v78 src0_sel:WORD_1
	v_cvt_pk_f32_fp8_e32 v[88:89], v79
	s_waitcnt lgkmcnt(0)
	v_pk_fma_f32 v[98:99], v[48:49], v[24:25], v[26:27] op_sel_hi:[0,1,1]
	s_waitcnt vmcnt(8)
	v_cvt_pk_f32_fp8_e32 v[24:25], v80
	v_pk_fma_f32 v[44:45], v[48:49], v[86:87], v[44:45] op_sel_hi:[0,1,1]
	v_cvt_pk_f32_fp8_sdwa v[26:27], v80 src0_sel:WORD_1
	v_cvt_pk_f32_fp8_e32 v[86:87], v81
	v_cvt_pk_f32_fp8_sdwa v[80:81], v81 src0_sel:WORD_1
	v_pk_fma_f32 v[50:51], v[48:49], v[24:25], v[50:51] op_sel_hi:[0,1,1]
	s_waitcnt vmcnt(7)
	v_cvt_pk_f32_fp8_e32 v[24:25], v82
	v_pk_fma_f32 v[38:39], v[48:49], v[86:87], v[38:39] op_sel_hi:[0,1,1]
	v_pk_fma_f32 v[80:81], v[48:49], v[80:81], v[30:31] op_sel_hi:[0,1,1]
	v_cvt_pk_f32_fp8_sdwa v[30:31], v82 src0_sel:WORD_1
	v_cvt_pk_f32_fp8_e32 v[86:87], v83
	v_cvt_pk_f32_fp8_sdwa v[82:83], v83 src0_sel:WORD_1
	v_cvt_pk_f32_fp8_sdwa v[78:79], v79 src0_sel:WORD_1
	v_pk_fma_f32 v[72:73], v[48:49], v[30:31], v[72:73] op_sel_hi:[0,1,1]
	v_pk_fma_f32 v[40:41], v[48:49], v[86:87], v[40:41] op_sel_hi:[0,1,1]
	v_pk_fma_f32 v[34:35], v[48:49], v[82:83], v[34:35] op_sel_hi:[0,1,1]
	v_pk_fma_f32 v[32:33], v[48:49], v[88:89], v[32:33] op_sel_hi:[0,1,1]
	v_pk_fma_f32 v[28:29], v[48:49], v[78:79], v[28:29] op_sel_hi:[0,1,1]
	v_pk_fma_f32 v[46:47], v[48:49], v[26:27], v[46:47] op_sel_hi:[0,1,1]
	v_pk_fma_f32 v[52:53], v[48:49], v[24:25], v[52:53] op_sel_hi:[0,1,1]
	global_load_dwordx2 v[78:79], v[84:85], off offset:1024
	v_lshl_add_u64 v[88:89], v[6:7], 0, s[16:17]
	global_load_dwordx2 v[84:85], v[84:85], off offset:1536
	s_waitcnt vmcnt(8)
; #define GAS __attribute__((address_space(1)))
; template <bool Y8, bool LAST>
; __device__ __forceinline__ void combine_ln2_phase(Frame& F, int layer) {
;     ...
;         for (int k = 0; k < 9; ++k) { size_t row; float gt;
;             if (k < 8) { row = (size_t)__shfl(myrow, tj * 8 + k); gt = __shfl(mygate, tj * 8 + k); }
;             else { row = (size_t)toff[N_EXPERTS] * 256 + t; gt = 1.0f; }
;             if constexpr (Y8) {
;                 const GAS u32x2* yp = (const GAS u32x2*)((const GAS unsigned char*)Y + row * D_MODEL) + lane;
; #pragma unroll
;                 for (int j = 0; j < 4; ++j) { const u32x2 y = yp[64 * j];
;                     const f32x2 p0 = __builtin_amdgcn_cvt_pk_f32_fp8((int)y.x, false), p1 = __builtin_amdgcn_cvt_pk_f32_fp8((int)y.x, true), p2 = __builtin_amdgcn_cvt_pk_f32_fp8((int)y.y, false), p3 = __builtin_amdgcn_cvt_pk_f32_fp8((int)y.y, true);
;                     a[j][0] += (f32x4){p0[0], p0[1], p1[0], p1[1]} * gt; a[j][1] += (f32x4){p2[0], p2[1], p3[0], p3[1]} * gt; }
;             } else {
;             const GAS u32x4* yp = (const GAS u32x4*)(Y + row * D_MODEL) + lane;
; #pragma unroll
;             for (int j = 0; j < 4; ++j) { const u32x4 y = yp[64 * j];
;                 a[j][0] += (f32x4){bflo(y.x), bfhi(y.x), bflo(y.y), bfhi(y.y)} * gt; a[j][1] += (f32x4){bflo(y.z), bfhi(y.z), bflo(y.w), bfhi(y.w)} * gt; } } }
;         float s = 0.f;
; #pragma unroll
;         for (int j = 0; j < 4; ++j) { const u32x4 xv = *(const GAS u32x4*)(X1B + (size_t)t * D_MODEL + 8 * lane + 512 * j);
;             a[j][0] += (f32x4){bflo(xv.x), bfhi(xv.x), bflo(xv.y), bfhi(xv.y)} * DN_ALPHA; a[j][1] += (f32x4){bflo(xv.z), bfhi(xv.z), bflo(xv.w), bfhi(xv.w)} * DN_ALPHA;
;             s += (a[j][0][0] + a[j][0][1]) + (a[j][0][2] + a[j][0][3]) + (a[j][1][0] + a[j][1][1]) + (a[j][1][2] + a[j][1][3]); }
	v_cvt_pk_f32_fp8_e32 v[30:31], v68
	v_cvt_pk_f32_fp8_sdwa v[82:83], v68 src0_sel:WORD_1
	v_cvt_pk_f32_fp8_e32 v[86:87], v69
	v_cvt_pk_f32_fp8_sdwa v[68:69], v69 src0_sel:WORD_1
	v_pk_fma_f32 v[54:55], v[48:49], v[30:31], v[54:55] op_sel_hi:[0,1,1]
	v_pk_fma_f32 v[70:71], v[48:49], v[82:83], v[70:71] op_sel_hi:[0,1,1]
	v_pk_fma_f32 v[42:43], v[48:49], v[86:87], v[42:43] op_sel_hi:[0,1,1]
	v_pk_fma_f32 v[36:37], v[48:49], v[68:69], v[36:37] op_sel_hi:[0,1,1]
	ds_bpermute_b32 v48, v67, v65
	global_load_dwordx4 v[24:27], v[88:89], off
	s_waitcnt vmcnt(6)
	v_cvt_pk_f32_fp8_e32 v[68:69], v94
	v_cvt_pk_f32_fp8_e32 v[86:87], v95
	v_cvt_pk_f32_fp8_sdwa v[30:31], v94 src0_sel:WORD_1
	v_cvt_pk_f32_fp8_sdwa v[82:83], v95 src0_sel:WORD_1
	s_waitcnt lgkmcnt(0)
	v_pk_fma_f32 v[68:69], v[48:49], v[68:69], v[98:99] op_sel_hi:[0,1,1]
	v_pk_fma_f32 v[86:87], v[48:49], v[86:87], v[32:33] op_sel_hi:[0,1,1]
	s_waitcnt vmcnt(5)
	v_cvt_pk_f32_fp8_e32 v[32:33], v92
	v_cvt_pk_f32_fp8_sdwa v[94:95], v92 src0_sel:WORD_1
	v_cvt_pk_f32_fp8_e32 v[98:99], v93
	v_cvt_pk_f32_fp8_sdwa v[92:93], v93 src0_sel:WORD_1
	v_pk_fma_f32 v[50:51], v[48:49], v[32:33], v[50:51] op_sel_hi:[0,1,1]
	v_pk_fma_f32 v[46:47], v[48:49], v[94:95], v[46:47] op_sel_hi:[0,1,1]
	s_waitcnt vmcnt(4)
	v_cvt_pk_f32_fp8_sdwa v[32:33], v96 src0_sel:WORD_1
	v_pk_fma_f32 v[80:81], v[48:49], v[92:93], v[80:81] op_sel_hi:[0,1,1]
	v_cvt_pk_f32_fp8_e32 v[92:93], v96
	v_cvt_pk_f32_fp8_sdwa v[94:95], v97 src0_sel:WORD_1
	v_cvt_pk_f32_fp8_e32 v[96:97], v97
	v_pk_fma_f32 v[72:73], v[48:49], v[32:33], v[72:73] op_sel_hi:[0,1,1]
	v_pk_fma_f32 v[52:53], v[48:49], v[92:93], v[52:53] op_sel_hi:[0,1,1]
	v_pk_fma_f32 v[92:93], v[48:49], v[94:95], v[34:35] op_sel_hi:[0,1,1]
	s_waitcnt vmcnt(3)
	v_cvt_pk_f32_fp8_sdwa v[32:33], v76 src0_sel:WORD_1
	v_cvt_pk_f32_fp8_e32 v[34:35], v76
	v_cvt_pk_f32_fp8_sdwa v[94:95], v77 src0_sel:WORD_1
	v_cvt_pk_f32_fp8_e32 v[76:77], v77
	v_pk_fma_f32 v[44:45], v[48:49], v[30:31], v[44:45] op_sel_hi:[0,1,1]
	v_pk_fma_f32 v[82:83], v[48:49], v[82:83], v[28:29] op_sel_hi:[0,1,1]
	global_load_dwordx4 v[28:31], v[88:89], off offset:1024
	v_pk_fma_f32 v[38:39], v[48:49], v[98:99], v[38:39] op_sel_hi:[0,1,1]
	v_pk_fma_f32 v[40:41], v[48:49], v[96:97], v[40:41] op_sel_hi:[0,1,1]
	v_pk_fma_f32 v[96:97], v[48:49], v[32:33], v[70:71] op_sel_hi:[0,1,1]
	v_pk_fma_f32 v[54:55], v[48:49], v[34:35], v[54:55] op_sel_hi:[0,1,1]
	v_pk_fma_f32 v[36:37], v[48:49], v[94:95], v[36:37] op_sel_hi:[0,1,1]
	v_pk_fma_f32 v[42:43], v[48:49], v[76:77], v[42:43] op_sel_hi:[0,1,1]
	v_cvt_pk_f32_fp8_e32 v[48:49], v90
	v_cvt_pk_f32_fp8_sdwa v[70:71], v90 src0_sel:WORD_1
	v_cvt_pk_f32_fp8_e32 v[76:77], v91
	v_cvt_pk_f32_fp8_sdwa v[90:91], v91 src0_sel:WORD_1
	v_pk_add_f32 v[48:49], v[68:69], v[48:49]
	v_pk_add_f32 v[44:45], v[44:45], v[70:71]
	v_cvt_pk_f32_fp8_e32 v[68:69], v74
	v_cvt_pk_f32_fp8_sdwa v[70:71], v74 src0_sel:WORD_1
	global_load_dwordx4 v[32:35], v[88:89], off offset:2048
	v_pk_add_f32 v[82:83], v[82:83], v[90:91]
	v_pk_add_f32 v[90:91], v[50:51], v[68:69]
	v_pk_add_f32 v[46:47], v[46:47], v[70:71]
	global_load_dwordx4 v[68:71], v[88:89], off offset:3072
	v_pk_add_f32 v[76:77], v[86:87], v[76:77]
	v_cvt_pk_f32_fp8_e32 v[86:87], v75
	v_cvt_pk_f32_fp8_sdwa v[74:75], v75 src0_sel:WORD_1
	s_waitcnt vmcnt(5)
	v_cvt_pk_f32_fp8_e32 v[50:51], v78
	v_pk_add_f32 v[38:39], v[38:39], v[86:87]
	v_pk_add_f32 v[74:75], v[80:81], v[74:75]
	v_cvt_pk_f32_fp8_sdwa v[80:81], v78 src0_sel:WORD_1
	v_cvt_pk_f32_fp8_e32 v[86:87], v79
	v_pk_add_f32 v[88:89], v[52:53], v[50:51]
	s_waitcnt vmcnt(4)
	v_cvt_pk_f32_fp8_sdwa v[50:51], v84 src0_sel:WORD_1
	v_pk_add_f32 v[72:73], v[72:73], v[80:81]
	v_pk_add_f32 v[80:81], v[40:41], v[86:87]
	v_cvt_pk_f32_fp8_e32 v[40:41], v84
	v_cvt_pk_f32_fp8_e32 v[52:53], v85
	v_cvt_pk_f32_fp8_sdwa v[84:85], v85 src0_sel:WORD_1
	v_cvt_pk_f32_fp8_sdwa v[78:79], v79 src0_sel:WORD_1
	v_pk_add_f32 v[86:87], v[54:55], v[40:41]
	v_pk_add_f32 v[94:95], v[42:43], v[52:53]
	v_pk_add_f32 v[84:85], v[36:37], v[84:85]
	v_pk_add_f32 v[78:79], v[92:93], v[78:79]
	v_pk_add_f32 v[92:93], v[96:97], v[50:51]
	s_waitcnt vmcnt(3)
	v_lshlrev_b32_e32 v36, 16, v24
	v_and_b32_e32 v37, 0xffff0000, v24
	v_lshlrev_b32_e32 v24, 16, v25
	v_and_b32_e32 v25, 0xffff0000, v25
	v_pk_fma_f32 v[52:53], v[24:25], s[4:5], v[44:45] op_sel_hi:[1,0,1]
	v_pk_fma_f32 v[54:55], v[36:37], s[4:5], v[48:49] op_sel_hi:[1,0,1]
	v_lshlrev_b32_e32 v24, 16, v26
	v_and_b32_e32 v25, 0xffff0000, v26
	v_lshlrev_b32_e32 v26, 16, v27
	v_and_b32_e32 v27, 0xffff0000, v27
	v_pk_fma_f32 v[48:49], v[26:27], s[4:5], v[82:83] op_sel_hi:[1,0,1]
	v_pk_fma_f32 v[50:51], v[24:25], s[4:5], v[76:77] op_sel_hi:[1,0,1]
	v_pk_mov_b32 v[24:25], v[54:55], v[52:53] op_sel:[1,0]
	v_mov_b32_e32 v26, v54
	v_mov_b32_e32 v27, v53
	v_pk_add_f32 v[24:25], v[24:25], v[26:27]
	v_mov_b32_e32 v26, v48
	v_mov_b32_e32 v27, v50
	v_mov_b32_e32 v36, v49
	v_mov_b32_e32 v37, v51
	v_pk_add_f32 v[26:27], v[26:27], v[36:37]
	v_add_f32_e32 v24, v24, v25
	v_add_f32_e32 v24, v27, v24
	v_add_f32_e32 v24, v26, v24
	v_add_f32_e32 v76, 0, v24
	s_waitcnt vmcnt(2)
	v_lshlrev_b32_e32 v24, 16, v28
	v_and_b32_e32 v25, 0xffff0000, v28
	v_lshlrev_b32_e32 v26, 16, v29
	v_and_b32_e32 v27, 0xffff0000, v29
	v_pk_fma_f32 v[44:45], v[26:27], s[4:5], v[46:47] op_sel_hi:[1,0,1]
	v_pk_fma_f32 v[46:47], v[24:25], s[4:5], v[90:91] op_sel_hi:[1,0,1]
	v_lshlrev_b32_e32 v24, 16, v30
	v_and_b32_e32 v25, 0xffff0000, v30
	v_lshlrev_b32_e32 v26, 16, v31
	v_and_b32_e32 v27, 0xffff0000, v31
	v_pk_fma_f32 v[40:41], v[26:27], s[4:5], v[74:75] op_sel_hi:[1,0,1]
	v_pk_fma_f32 v[42:43], v[24:25], s[4:5], v[38:39] op_sel_hi:[1,0,1]
	v_pk_mov_b32 v[24:25], v[46:47], v[44:45] op_sel:[1,0]
	v_mov_b32_e32 v26, v46
	v_mov_b32_e32 v27, v45
	v_pk_add_f32 v[24:25], v[24:25], v[26:27]
	v_mov_b32_e32 v26, v40
	v_mov_b32_e32 v27, v42
	v_mov_b32_e32 v28, v41
	v_mov_b32_e32 v29, v43
	v_pk_add_f32 v[24:25], v[24:25], v[24:25] op_sel:[0,1] op_sel_hi:[1,0]
	v_pk_add_f32 v[26:27], v[26:27], v[28:29]
	s_waitcnt vmcnt(0)
; #define GAS __attribute__((address_space(1)))
; template <bool Y8, bool LAST>
; __device__ __forceinline__ void combine_ln2_phase(Frame& F, int layer) {
;     ...
;         for (int j = 0; j < 4; ++j) { const u32x4 xv = *(const GAS u32x4*)(X1B + (size_t)t * D_MODEL + 8 * lane + 512 * j);
;             a[j][0] += (f32x4){bflo(xv.x), bfhi(xv.x), bflo(xv.y), bfhi(xv.y)} * DN_ALPHA; a[j][1] += (f32x4){bflo(xv.z), bfhi(xv.z), bflo(xv.w), bfhi(xv.w)} * DN_ALPHA;
;             s += (a[j][0][0] + a[j][0][1]) + (a[j][0][2] + a[j][0][3]) + (a[j][1][0] + a[j][1][1]) + (a[j][1][2] + a[j][1][3]); }
;         const float mean = wave_sum(s) * (1.0f / D_MODEL); float s2 = 0.f;
; #pragma unroll
;         for (int j = 0; j < 4; ++j) { a[j][0] = a[j][0] - mean; a[j][1] = a[j][1] - mean;
;             s2 += (a[j][0][0] * a[j][0][0] + a[j][0][1] * a[j][0][1]) + (a[j][0][2] * a[j][0][2] + a[j][0][3] * a[j][0][3]) + (a[j][1][0] * a[j][1][0] + a[j][1][1] * a[j][1][1]) + (a[j][1][2] * a[j][1][2] + a[j][1][3] * a[j][1][3]); }
;         const float rstd = rsqrtf(wave_sum(s2) * (1.0f / D_MODEL) + LN_EPS);
	v_lshlrev_b32_e32 v30, 16, v70
	v_pk_add_f32 v[24:25], v[26:27], v[24:25] op_sel:[1,0] op_sel_hi:[0,1]
	v_pk_add_f32 v[74:75], v[26:27], v[24:25]
	v_lshlrev_b32_e32 v24, 16, v32
	v_and_b32_e32 v25, 0xffff0000, v32
	v_lshlrev_b32_e32 v26, 16, v33
	v_and_b32_e32 v27, 0xffff0000, v33
	v_pk_fma_f32 v[36:37], v[26:27], s[4:5], v[72:73] op_sel_hi:[1,0,1]
	v_pk_fma_f32 v[38:39], v[24:25], s[4:5], v[88:89] op_sel_hi:[1,0,1]
	v_lshlrev_b32_e32 v24, 16, v34
	v_and_b32_e32 v25, 0xffff0000, v34
	v_lshlrev_b32_e32 v26, 16, v35
	v_and_b32_e32 v27, 0xffff0000, v35
	v_pk_fma_f32 v[32:33], v[26:27], s[4:5], v[78:79] op_sel_hi:[1,0,1]
	v_pk_fma_f32 v[34:35], v[24:25], s[4:5], v[80:81] op_sel_hi:[1,0,1]
	v_lshlrev_b32_e32 v24, 16, v68
	v_and_b32_e32 v25, 0xffff0000, v68
	v_lshlrev_b32_e32 v26, 16, v69
	v_and_b32_e32 v27, 0xffff0000, v69
	v_pk_fma_f32 v[26:27], v[26:27], s[4:5], v[92:93] op_sel_hi:[1,0,1]
	v_pk_fma_f32 v[28:29], v[24:25], s[4:5], v[86:87] op_sel_hi:[1,0,1]
	v_add_f32_e32 v72, v38, v39
	v_add_f32_e32 v78, v36, v37
	v_and_b32_e32 v31, 0xffff0000, v70
	v_lshlrev_b32_e32 v24, 16, v71
	v_and_b32_e32 v25, 0xffff0000, v71
	v_mov_b32_e32 v68, v34
	v_mov_b32_e32 v69, v28
	v_mov_b32_e32 v70, v35
	v_mov_b32_e32 v71, v29
	v_mov_b32_e32 v73, v26
	v_mov_b32_e32 v79, v27
	v_pk_fma_f32 v[30:31], v[30:31], s[4:5], v[94:95] op_sel_hi:[1,0,1]
	v_pk_add_f32 v[68:69], v[68:69], v[70:71]
	v_pk_add_f32 v[70:71], v[72:73], v[78:79]
	v_pk_fma_f32 v[24:25], v[24:25], s[4:5], v[84:85] op_sel_hi:[1,0,1]
	v_pk_add_f32 v[68:69], v[68:69], v[70:71]
	v_mov_b32_e32 v70, v32
	v_mov_b32_e32 v71, v30
	v_mov_b32_e32 v72, v33
	v_mov_b32_e32 v73, v31
	v_pk_add_f32 v[70:71], v[70:71], v[72:73]
	v_mov_b32_e32 v77, v24
	v_mov_b32_e32 v75, v25
	v_pk_add_f32 v[68:69], v[70:71], v[68:69]
	v_pk_add_f32 v[70:71], v[76:77], v[74:75]
	s_nop 0
	v_pk_add_f32 v[68:69], v[70:71], v[68:69]
	s_nop 0
	v_add_f32_e32 v67, v68, v69
	v_cndmask_b32_e32 v68, v3, v58, vcc
	v_lshlrev_b32_e32 v100, 2, v68
	ds_bpermute_b32 v68, v100, v67
	v_cmp_lt_i32_e32 vcc, v59, v57
	s_waitcnt lgkmcnt(0)
	v_add_f32_e32 v67, v67, v68
	v_cndmask_b32_e32 v68, v3, v59, vcc
	v_lshlrev_b32_e32 v101, 2, v68
	ds_bpermute_b32 v68, v101, v67
	v_cmp_lt_i32_e32 vcc, v60, v57
	s_waitcnt lgkmcnt(0)
	v_add_f32_e32 v67, v67, v68
	v_cndmask_b32_e32 v68, v3, v60, vcc
	v_lshlrev_b32_e32 v102, 2, v68
	ds_bpermute_b32 v68, v102, v67
	v_cmp_lt_i32_e32 vcc, v61, v57
	s_waitcnt lgkmcnt(0)
	v_add_f32_e32 v67, v67, v68
	v_cndmask_b32_e32 v68, v3, v61, vcc
	v_lshlrev_b32_e32 v103, 2, v68
	ds_bpermute_b32 v68, v103, v67
	v_cmp_lt_i32_e32 vcc, v62, v57
	s_waitcnt lgkmcnt(0)
	v_add_f32_e32 v67, v67, v68
	v_cndmask_b32_e32 v68, v3, v62, vcc
	v_lshlrev_b32_e32 v104, 2, v68
	ds_bpermute_b32 v68, v104, v67
	v_cmp_lt_i32_e32 vcc, v63, v57
	s_waitcnt lgkmcnt(0)
	v_add_f32_e32 v67, v67, v68
	v_cndmask_b32_e32 v68, v3, v63, vcc
	v_lshlrev_b32_e32 v105, 2, v68
	ds_bpermute_b32 v68, v105, v67
	s_waitcnt lgkmcnt(0)
	v_add_f32_e32 v67, v67, v68
	v_fmamk_f32 v55, v67, 0xba000000, v55
	v_fmac_f32_e32 v54, 0xba000000, v67
	v_fmamk_f32 v53, v67, 0xba000000, v53
	v_fmac_f32_e32 v52, 0xba000000, v67
	v_pk_mul_f32 v[68:69], v[52:53], v[52:53]
	v_pk_mul_f32 v[70:71], v[54:55], v[54:55]
	v_fmamk_f32 v51, v67, 0xba000000, v51
	v_fmac_f32_e32 v50, 0xba000000, v67
	v_fmamk_f32 v49, v67, 0xba000000, v49
	v_fmac_f32_e32 v48, 0xba000000, v67
	v_pk_mov_b32 v[72:73], v[70:71], v[68:69] op_sel:[1,0]
	v_mov_b32_e32 v71, v69
	v_pk_add_f32 v[68:69], v[72:73], v[70:71]
	v_pk_mul_f32 v[70:71], v[48:49], v[48:49]
	v_pk_mul_f32 v[72:73], v[50:51], v[50:51]
	v_mov_b32_e32 v74, v70
	v_mov_b32_e32 v75, v72
	v_mov_b32_e32 v72, v71
	v_pk_add_f32 v[68:69], v[68:69], v[68:69] op_sel:[0,1] op_sel_hi:[1,0]
	v_pk_add_f32 v[70:71], v[74:75], v[72:73]
	v_fmamk_f32 v47, v67, 0xba000000, v47
	v_pk_add_f32 v[68:69], v[70:71], v[68:69] op_sel:[1,0] op_sel_hi:[0,1]
	v_fmac_f32_e32 v46, 0xba000000, v67
	v_fmamk_f32 v45, v67, 0xba000000, v45
	v_fmac_f32_e32 v44, 0xba000000, v67
	v_pk_add_f32 v[84:85], v[70:71], v[68:69]
	v_pk_mul_f32 v[68:69], v[44:45], v[44:45]
	v_pk_mul_f32 v[70:71], v[46:47], v[46:47]
	v_fmamk_f32 v43, v67, 0xba000000, v43
	v_fmac_f32_e32 v42, 0xba000000, v67
	v_fmamk_f32 v41, v67, 0xba000000, v41
	v_fmac_f32_e32 v40, 0xba000000, v67
	v_pk_mov_b32 v[72:73], v[70:71], v[68:69] op_sel:[1,0]
	v_mov_b32_e32 v71, v69
	v_pk_add_f32 v[68:69], v[72:73], v[70:71]
	v_pk_mul_f32 v[70:71], v[40:41], v[40:41]
	v_pk_mul_f32 v[72:73], v[42:43], v[42:43]
	v_mov_b32_e32 v74, v70
	v_mov_b32_e32 v75, v72
	v_mov_b32_e32 v72, v71
	v_pk_add_f32 v[68:69], v[68:69], v[68:69] op_sel:[0,1] op_sel_hi:[1,0]
	v_pk_add_f32 v[70:71], v[74:75], v[72:73]
	v_fmac_f32_e32 v38, 0xba000000, v67
	v_pk_add_f32 v[68:69], v[70:71], v[68:69] op_sel:[1,0] op_sel_hi:[0,1]
	v_pk_add_f32 v[86:87], v[70:71], v[68:69]
	v_fmamk_f32 v39, v67, 0xba000000, v39
	v_fmac_f32_e32 v36, 0xba000000, v67
	v_mul_f32_e32 v68, v38, v38
	v_fmamk_f32 v37, v67, 0xba000000, v37
	v_pk_fma_f32 v[88:89], v[38:39], v[38:39], v[68:69] op_sel_hi:[1,1,0]
	v_mul_f32_e32 v68, v36, v36
	v_pk_fma_f32 v[90:91], v[36:37], v[36:37], v[68:69] op_sel_hi:[1,1,0]
	v_fmamk_f32 v35, v67, 0xba000000, v35
	v_fmamk_f32 v29, v67, 0xba000000, v29
	v_fmac_f32_e32 v34, 0xba000000, v67
	v_fmac_f32_e32 v28, 0xba000000, v67
	v_fmamk_f32 v27, v67, 0xba000000, v27
	v_fmac_f32_e32 v26, 0xba000000, v67
	v_mov_b32_e32 v98, v29
	v_mov_b32_e32 v99, v35
	v_mul_f32_e32 v88, v26, v26
	v_mul_f32_e32 v90, v27, v27
	v_mov_b32_e32 v96, v28
	v_mov_b32_e32 v97, v34
	v_pk_mul_f32 v[98:99], v[98:99], v[98:99]
	v_fmamk_f32 v33, v67, 0xba000000, v33
	v_fmamk_f32 v31, v67, 0xba000000, v31
	v_pk_fma_f32 v[96:97], v[96:97], v[96:97], v[98:99]
	v_pk_add_f32 v[88:89], v[88:89], v[90:91]
	v_fmac_f32_e32 v32, 0xba000000, v67
	v_fmac_f32_e32 v30, 0xba000000, v67
	v_pk_add_f32 v[88:89], v[96:97], v[88:89]
	v_mov_b32_e32 v96, v31
	v_mov_b32_e32 v97, v33
	v_fmamk_f32 v25, v67, 0xba000000, v25
	v_fmac_f32_e32 v24, 0xba000000, v67
	v_mov_b32_e32 v90, v30
	v_mov_b32_e32 v91, v32
	v_pk_mul_f32 v[96:97], v[96:97], v[96:97]
	v_mul_f32_e32 v92, v24, v24
	v_mul_f32_e32 v94, v25, v25
	v_pk_fma_f32 v[90:91], v[90:91], v[90:91], v[96:97]
	v_mov_b32_e32 v93, v84
	v_mov_b32_e32 v95, v86
	v_pk_add_f32 v[88:89], v[90:91], v[88:89]
	v_pk_add_f32 v[84:85], v[92:93], v[94:95]
	s_nop 0
	v_pk_add_f32 v[84:85], v[88:89], v[84:85]
	s_nop 0
	v_add_f32_e32 v67, v84, v85
	ds_bpermute_b32 v84, v100, v67
	s_waitcnt lgkmcnt(0)
; #define GAS __attribute__((address_space(1)))
; __device__ __forceinline__ unsigned cvt_pk_bf16(float lo, float hi) { unsigned r; asm volatile("v_cvt_pk_bf16_f32 %0, %1, %2" : "=v"(r) : "v"(lo), "v"(hi)); return r; }
; template <bool Y8, bool LAST>
; __device__ __forceinline__ void combine_ln2_phase(Frame& F, int layer) {
;     ...
;         const float rstd = rsqrtf(wave_sum(s2) * (1.0f / D_MODEL) + LN_EPS);
; #pragma unroll
;         for (int j = 0; j < 4; ++j) { const int c = 8 * lane + 512 * j;
;             const f32x4 o0 = a[j][0] * rstd * *(const GAS f32x4*)(g2 + c) + *(const GAS f32x4*)(b2 + c), o1 = a[j][1] * rstd * *(const GAS f32x4*)(g2 + c + 4) + *(const GAS f32x4*)(b2 + c + 4);
;             if constexpr (LAST) { *(GAS f32x4*)(OUT + (size_t)t * D_MODEL + c) = o0; *(GAS f32x4*)(OUT + (size_t)t * D_MODEL + c + 4) = o1; }
;             else {
;             u32x4 wv; wv.x = cvt_pk_bf16(o0[0], o0[1]); wv.y = cvt_pk_bf16(o0[2], o0[3]); wv.z = cvt_pk_bf16(o1[0], o1[1]); wv.w = cvt_pk_bf16(o1[2], o1[3]);
;             *(GAS u32x4*)(XB + (size_t)t * D_MODEL + c) = wv;
;             u32x2 w8; { int q = __builtin_amdgcn_cvt_pk_fp8_f32(o0[0], o0[1], 0, false); q = __builtin_amdgcn_cvt_pk_fp8_f32(o0[2], o0[3], q, true); w8.x = (unsigned)q;
;                         q = __builtin_amdgcn_cvt_pk_fp8_f32(o1[0], o1[1], 0, false); q = __builtin_amdgcn_cvt_pk_fp8_f32(o1[2], o1[3], q, true); w8.y = (unsigned)q; }
;             *(GAS u32x2*)(XB8 + (size_t)t * D_MODEL + c) = w8; } }
	v_add_f32_e32 v67, v67, v84
	ds_bpermute_b32 v84, v101, v67
	s_waitcnt lgkmcnt(0)
	v_add_f32_e32 v67, v67, v84
	ds_bpermute_b32 v84, v102, v67
	s_waitcnt lgkmcnt(0)
	v_add_f32_e32 v67, v67, v84
	ds_bpermute_b32 v84, v103, v67
	s_waitcnt lgkmcnt(0)
	v_add_f32_e32 v67, v67, v84
	ds_bpermute_b32 v84, v104, v67
	s_waitcnt lgkmcnt(0)
	v_add_f32_e32 v67, v67, v84
	ds_bpermute_b32 v84, v105, v67
	s_waitcnt lgkmcnt(0)
	v_add_f32_e32 v67, v67, v84
	v_fmamk_f32 v67, v67, 0x3a000000, v64
	v_mul_f32_e32 v84, 0x4b800000, v67
	v_cmp_gt_f32_e32 vcc, s19, v67
	s_nop 1
	v_cndmask_b32_e32 v67, v67, v84, vcc
	v_rsq_f32_e32 v67, v67
	s_nop 0
	v_mul_f32_e32 v84, 0x45800000, v67
	v_cndmask_b32_e32 v84, v67, v84, vcc
	v_pk_mul_f32 v[54:55], v[54:55], v[84:85] op_sel_hi:[1,0]
	v_pk_mul_f32 v[50:51], v[50:51], v[84:85] op_sel_hi:[1,0]
	v_pk_fma_f32 v[54:55], v[132:133], v[54:55], v[140:141]
	v_pk_fma_f32 v[50:51], v[128:129], v[50:51], v[136:137]
	v_mov_b32_e32 v68, 0
	v_mov_b32_e32 v69, 0
	v_cvt_pk_fp8_f32 v68, v54, v55
	v_cvt_pk_fp8_f32 v69, v50, v51
	v_pk_mul_f32 v[52:53], v[52:53], v[84:85] op_sel_hi:[1,0]
	v_pk_mul_f32 v[48:49], v[48:49], v[84:85] op_sel_hi:[1,0]
	v_pk_fma_f32 v[52:53], v[134:135], v[52:53], v[142:143]
	v_pk_fma_f32 v[70:71], v[130:131], v[48:49], v[138:139]
	v_cvt_pk_fp8_f32 v68, v52, v53 op_sel:[0,0,1]
	v_cvt_pk_fp8_f32 v69, v70, v71 op_sel:[0,0,1]
	v_lshl_add_u64 v[76:77], v[20:21], 0, s[16:17]
	v_lshl_add_u64 v[78:79], v[22:23], 0, s[14:15]
	v_cvt_pk_bf16_f32 v48, v54, v55
	v_cvt_pk_bf16_f32 v49, v52, v53
	v_cvt_pk_bf16_f32 v50, v50, v51
	v_cvt_pk_bf16_f32 v51, v70, v71
	global_store_dwordx4 v[76:77], v[48:51], off
	global_store_dwordx2 v[78:79], v[68:69], off
	s_nop 0
	v_pk_mul_f32 v[46:47], v[46:47], v[84:85] op_sel_hi:[1,0]
	v_pk_mul_f32 v[44:45], v[44:45], v[84:85] op_sel_hi:[1,0]
	v_pk_mul_f32 v[42:43], v[42:43], v[84:85] op_sel_hi:[1,0]
	v_pk_mul_f32 v[40:41], v[40:41], v[84:85] op_sel_hi:[1,0]
	v_pk_mul_f32 v[38:39], v[38:39], v[84:85] op_sel_hi:[1,0]
	v_pk_mul_f32 v[36:37], v[36:37], v[84:85] op_sel_hi:[1,0]
	v_pk_mul_f32 v[34:35], v[34:35], v[84:85] op_sel_hi:[1,0]
	v_pk_mul_f32 v[32:33], v[32:33], v[84:85] op_sel_hi:[1,0]
	v_pk_mul_f32 v[28:29], v[28:29], v[84:85] op_sel_hi:[1,0]
	v_pk_mul_f32 v[26:27], v[26:27], v[84:85] op_sel_hi:[1,0]
	v_pk_mul_f32 v[30:31], v[30:31], v[84:85] op_sel_hi:[1,0]
	v_pk_mul_f32 v[24:25], v[24:25], v[84:85] op_sel_hi:[1,0]
	s_cselect_b64 s[14:15], -1, 0
	v_pk_fma_f32 v[44:45], v[150:151], v[44:45], v[146:147]
	v_pk_fma_f32 v[46:47], v[148:149], v[46:47], v[144:145]
	v_pk_fma_f32 v[42:43], v[152:153], v[42:43], v[156:157]
	v_mov_b32_e32 v50, 0
	v_mov_b32_e32 v51, 0
	v_cvt_pk_fp8_f32 v50, v46, v47
	v_cvt_pk_fp8_f32 v51, v42, v43
	v_pk_fma_f32 v[48:49], v[154:155], v[40:41], v[158:159]
	v_cvt_pk_bf16_f32 v40, v46, v47
	v_cvt_pk_fp8_f32 v50, v44, v45 op_sel:[0,0,1]
	v_cvt_pk_fp8_f32 v51, v48, v49 op_sel:[0,0,1]
	v_cvt_pk_bf16_f32 v41, v44, v45
	v_cvt_pk_bf16_f32 v42, v42, v43
	v_cvt_pk_bf16_f32 v43, v48, v49
	global_store_dwordx4 v[76:77], v[40:43], off offset:1024
	global_store_dwordx2 v[78:79], v[50:51], off offset:512
	s_nop 0
	v_pk_fma_f32 v[36:37], v[166:167], v[36:37], v[162:163]
	v_pk_fma_f32 v[38:39], v[164:165], v[38:39], v[160:161]
	v_pk_fma_f32 v[34:35], v[168:169], v[34:35], v[172:173]
	v_mov_b32_e32 v42, 0
	v_mov_b32_e32 v43, 0
	v_cvt_pk_fp8_f32 v42, v38, v39
	v_cvt_pk_fp8_f32 v43, v34, v35
	v_pk_fma_f32 v[40:41], v[170:171], v[32:33], v[174:175]
	v_cvt_pk_bf16_f32 v32, v38, v39
	v_cvt_pk_fp8_f32 v42, v36, v37 op_sel:[0,0,1]
	v_cvt_pk_fp8_f32 v43, v40, v41 op_sel:[0,0,1]
	v_cvt_pk_bf16_f32 v33, v36, v37
	v_cvt_pk_bf16_f32 v34, v34, v35
	v_cvt_pk_bf16_f32 v35, v40, v41
	global_store_dwordx4 v[76:77], v[32:35], off offset:2048
	global_store_dwordx2 v[78:79], v[42:43], off offset:1024
	s_nop 0
	v_pk_fma_f32 v[26:27], v[26:27], v[182:183], v[178:179]
	v_pk_fma_f32 v[28:29], v[28:29], v[180:181], v[176:177]
	v_pk_fma_f32 v[30:31], v[30:31], v[184:185], v[188:189]
	v_mov_b32_e32 v34, 0
	v_mov_b32_e32 v35, 0
	v_cvt_pk_fp8_f32 v34, v28, v29
	v_cvt_pk_fp8_f32 v35, v30, v31
	v_pk_fma_f32 v[32:33], v[24:25], v[186:187], v[190:191]
	v_cvt_pk_bf16_f32 v24, v28, v29
	v_cvt_pk_fp8_f32 v34, v26, v27 op_sel:[0,0,1]
	v_cvt_pk_fp8_f32 v35, v32, v33 op_sel:[0,0,1]
	v_cvt_pk_bf16_f32 v25, v26, v27
	v_cvt_pk_bf16_f32 v26, v30, v31
	v_cvt_pk_bf16_f32 v27, v32, v33
	global_store_dwordx4 v[76:77], v[24:27], off offset:3072
	global_store_dwordx2 v[78:79], v[34:35], off offset:1536
	s_branch .LBB0_2033

; #define GAS __attribute__((address_space(1)))
; #define LAS __attribute__((address_space(3)))
; #define PHASE_ARGS() CArgsP ap = (CArgsP)__builtin_amdgcn_kernarg_segment_ptr(); asm volatile("" : "+s"(ap))
; #define PHASE_IDS() int tid = threadIdx.x; asm volatile("" : "+v"(tid)); const int lane = tid & 63, w = __builtin_amdgcn_readfirstlane(tid >> 6); (void)lane; (void)w
; template <bool Y8, bool LAST>
; __device__ __forceinline__ void combine_ln2_phase(Frame& F, int layer) {
;     PHASE_ARGS(); GAS float* OUT = (GAS float*)(GAS float*)ap->out;
;     const GAS bf16_t* Y = (const GAS bf16_t*)(F.ws + WS_Y); const GAS bf16_t* X1B = (const GAS bf16_t*)(F.ws + WS_X1B); GAS bf16_t* XB = (GAS bf16_t*)(F.ws + WS_XB); GAS unsigned char* XB8 = F.ws + WS_XB8;
;     const GAS float* g2 = GIN(18) + (size_t)layer * D_MODEL; const GAS float* b2 = GIN(19) + (size_t)layer * D_MODEL;
;     const GAS int* PE = (const GAS int*)(F.ws + WS_PE); const GAS int* PP = (const GAS int*)(F.ws + WS_PP); const GAS float* PG = (const GAS float*)(F.ws + WS_PG);
;     const LAS int* toff = (const LAS int*)(F.lds + LDS_TAB);
;     PHASE_IDS();
;     const int gw = F.bid * 8 + w, NGW = F.G * 8;
;     for (int tb = gw; tb < T; tb += 8 * NGW) {
;         int myrow = 0; float mygate = 0.f;
;         { const int tl = tb + (lane >> 3) * NGW; if (tl < T) { const int e = PE[(size_t)tl * 8 + (lane & 7)]; myrow = toff[e] * 256 + PP[(size_t)tl * 8 + (lane & 7)]; mygate = PG[(size_t)tl * 8 + (lane & 7)]; } }
;     ...
;         for (int j = 0; j < 4; ++j) { const int c = 8 * lane + 512 * j;
;             const f32x4 o0 = a[j][0] * rstd * *(const GAS f32x4*)(g2 + c) + *(const GAS f32x4*)(b2 + c), o1 = a[j][1] * rstd * *(const GAS f32x4*)(g2 + c + 4) + *(const GAS f32x4*)(b2 + c + 4);
.LBB0_3255:
	s_or_b64 exec, exec, s[6:7]
	v_readlane_b32 s0, v254, 1
	v_readlane_b32 s1, v254, 2
	s_waitcnt lgkmcnt(0)
	s_barrier
	s_nop 0
	v_writelane_b32 v254, s0, 1
	s_nop 1
	v_writelane_b32 v254, s1, 2
	v_readfirstlane_b32 s0, v0
	v_readlane_b32 s1, v254, 0
	s_ashr_i32 s0, s0, 6
	s_lshl_b32 s1, s1, 3
	s_add_i32 s16, s0, s1
	s_cmpk_gt_i32 s16, 0x3fff
	s_cbranch_scc1 .LBB0_3264
	v_readlane_b32 s0, v254, 1
	v_readlane_b32 s1, v254, 2
	s_load_dwordx4 s[20:23], s[0:1], 0x90
	s_load_dwordx2 s[2:3], s[0:1], 0xa0
	s_add_u32 s0, s10, 0x35300000
	s_addc_u32 s1, s11, 0
	s_add_u32 s6, s10, 0x35400000
	s_addc_u32 s7, s11, 0
	s_add_u32 s8, s10, 0x35500000
	s_addc_u32 s9, s11, 0
	s_add_i32 s17, s19, 0x24000
	s_lshl_b32 s18, s12, 3
	s_waitcnt lgkmcnt(0)
	s_add_u32 s14, s22, 0x2000
	v_and_b32_e32 v6, 63, v0
	s_addc_u32 s15, s23, 0
	v_mov_b32_e32 v25, 0
	v_lshlrev_b32_e32 v24, 3, v6
	v_mbcnt_hi_u32_b32 v58, -1, v22
	s_add_u32 s20, s20, 0x2000
	v_lshlrev_b32_e32 v4, 4, v6
	v_mov_b32_e32 v5, v25
	v_lshlrev_b32_e32 v10, 5, v6
	v_or_b32_e32 v26, 0x400, v24
	v_or_b32_e32 v28, 0x600, v24
	v_lshlrev_b32_e32 v22, 2, v58
	s_addc_u32 s21, s21, 0
	v_bfe_u32 v1, v0, 3, 3
	v_lshl_add_u64 v[2:3], s[10:11], 0, v[24:25]
	s_mov_b64 s[22:23], 0x3fb00000
	v_lshl_add_u64 v[4:5], s[10:11], 0, v[4:5]
	s_mov_b64 s[10:11], 0x31300000
	v_mov_b32_e32 v11, v25
	v_or_b32_e32 v12, 0x800, v10
	v_mov_b32_e32 v13, v25
	v_lshlrev_b32_e32 v16, 2, v26
	v_mov_b32_e32 v17, v25
	v_lshlrev_b32_e32 v20, 2, v28
	v_mov_b32_e32 v21, v25
	v_and_b32_e32 v59, 0x100, v22
	v_and_b32_e32 v22, 64, v58
	v_mul_lo_u32 v1, v1, s18
	v_and_b32_e32 v0, 7, v0
	v_lshl_add_u64 v[2:3], v[2:3], 0, s[22:23]
	s_add_i32 s19, s19, 0x24100
	v_lshl_add_u64 v[4:5], v[4:5], 0, s[10:11]
	s_lshl_b32 s11, s12, 6
	v_lshl_add_u64 v[6:7], s[20:21], 0, v[10:11]
	v_lshl_add_u64 v[8:9], s[14:15], 0, v[10:11]
	v_lshl_add_u64 v[10:11], s[20:21], 0, v[12:13]
	v_lshl_add_u64 v[12:13], s[14:15], 0, v[12:13]
	v_lshl_add_u64 v[14:15], s[20:21], 0, v[16:17]
	v_lshl_add_u64 v[16:17], s[14:15], 0, v[16:17]
	v_lshl_add_u64 v[18:19], s[20:21], 0, v[20:21]
	v_lshl_add_u64 v[20:21], s[14:15], 0, v[20:21]
	s_movk_i32 s20, 0x4000
	s_mov_b32 s10, 0x3fb504f3
	v_mov_b32_e32 v54, 0x3727c5ac
	s_mov_b32 s21, 0x800000
	v_lshlrev_b32_e32 v55, 2, v24
	v_lshlrev_b32_e32 v56, 2, v26
	v_lshlrev_b32_e32 v57, 2, v28
	v_add_u32_e32 v60, 64, v22
	v_xor_b32_e32 v61, 1, v58
	v_xor_b32_e32 v62, 2, v58
	v_xor_b32_e32 v63, 4, v58
	v_xor_b32_e32 v64, 8, v58
	v_xor_b32_e32 v65, 16, v58
	v_xor_b32_e32 v66, 32, v58
	global_load_dwordx4 v[128:131], v[6:7], off offset:16
	global_load_dwordx4 v[132:135], v[6:7], off
	global_load_dwordx4 v[136:139], v[8:9], off offset:16
	global_load_dwordx4 v[140:143], v[8:9], off
	global_load_dwordx4 v[144:147], v[12:13], off
	global_load_dwordx4 v[148:151], v[10:11], off
	global_load_dwordx4 v[152:155], v[10:11], off offset:16
	global_load_dwordx4 v[156:159], v[12:13], off offset:16
	global_load_dwordx4 v[160:163], v[16:17], off
	global_load_dwordx4 v[164:167], v[14:15], off
	global_load_dwordx4 v[168:171], v[14:15], off offset:16
	global_load_dwordx4 v[172:175], v[16:17], off offset:16
	global_load_dwordx4 v[176:179], v[20:21], off
	global_load_dwordx4 v[180:183], v[18:19], off
	global_load_dwordx4 v[184:187], v[18:19], off offset:16
	global_load_dwordx4 v[188:191], v[20:21], off offset:16
	s_waitcnt vmcnt(0)
	s_branch .LBB0_3258

; template <bool Y8, bool LAST>
; __device__ __forceinline__ void combine_ln2_phase(Frame& F, int layer) {
;     ...
;     for (int tb = gw; tb < T; tb += 8 * NGW) {
;         int myrow = 0; float mygate = 0.f;
;         { const int tl = tb + (lane >> 3) * NGW; if (tl < T) { const int e = PE[(size_t)tl * 8 + (lane & 7)]; myrow = toff[e] * 256 + PP[(size_t)tl * 8 + (lane & 7)]; mygate = PG[(size_t)tl * 8 + (lane & 7)]; } }
.LBB0_3258:
	v_add_u32_e32 v22, s16, v1
	v_cmp_gt_i32_e32 vcc, s20, v22
	s_waitcnt vmcnt(0)
	v_mov_b32_e32 v67, 0
	v_mov_b32_e32 v68, 0
	s_and_saveexec_b64 s[12:13], vcc
	s_cbranch_execz .LBB0_3260
	v_ashrrev_i32_e32 v23, 31, v22
	v_lshlrev_b64 v[22:23], 5, v[22:23]
	v_lshl_or_b32 v22, v0, 2, v22
	v_lshl_add_u64 v[24:25], s[0:1], 0, v[22:23]
	global_load_dword v26, v[24:25], off
	v_lshl_add_u64 v[24:25], s[6:7], 0, v[22:23]
	v_lshl_add_u64 v[22:23], s[8:9], 0, v[22:23]
	global_load_dword v27, v[24:25], off
	global_load_dword v67, v[22:23], off
	s_waitcnt vmcnt(2)
	v_lshl_add_u32 v22, v26, 2, s17
	ds_read_b32 v22, v22
	s_waitcnt vmcnt(0) lgkmcnt(0)
	v_lshl_add_u32 v68, v22, 8, v27

; #define GAS __attribute__((address_space(1)))
; template <bool Y8, bool LAST>
; __device__ __forceinline__ void combine_ln2_phase(Frame& F, int layer) {
;     ...
;       for (int tj = 0; tj < 8; ++tj) { const int t = tb + tj * NGW; if (t >= T) break;
;         f32x4 a[4][2];
; #pragma unroll
;         for (int j = 0; j < 4; ++j) { a[j][0] = (f32x4){0.f, 0.f, 0.f, 0.f}; a[j][1] = (f32x4){0.f, 0.f, 0.f, 0.f}; }
; #pragma unroll
;         for (int k = 0; k < 9; ++k) { size_t row; float gt;
;             if (k < 8) { row = (size_t)__shfl(myrow, tj * 8 + k); gt = __shfl(mygate, tj * 8 + k); }
;             else { row = (size_t)toff[N_EXPERTS] * 256 + t; gt = 1.0f; }
;             if constexpr (Y8) {
;                 const GAS u32x2* yp = (const GAS u32x2*)((const GAS unsigned char*)Y + row * D_MODEL) + lane;
; #pragma unroll
;                 for (int j = 0; j < 4; ++j) { const u32x2 y = yp[64 * j];
;                     const f32x2 p0 = __builtin_amdgcn_cvt_pk_f32_fp8((int)y.x, false), p1 = __builtin_amdgcn_cvt_pk_f32_fp8((int)y.x, true), p2 = __builtin_amdgcn_cvt_pk_f32_fp8((int)y.y, false), p3 = __builtin_amdgcn_cvt_pk_f32_fp8((int)y.y, true);
;                     a[j][0] += (f32x4){p0[0], p0[1], p1[0], p1[1]} * gt; a[j][1] += (f32x4){p2[0], p2[1], p3[0], p3[1]} * gt; }
;             } else {
;             const GAS u32x4* yp = (const GAS u32x4*)(Y + row * D_MODEL) + lane;
; #pragma unroll
;             for (int j = 0; j < 4; ++j) { const u32x4 y = yp[64 * j];
;                 a[j][0] += (f32x4){bflo(y.x), bfhi(y.x), bflo(y.y), bfhi(y.y)} * gt; a[j][1] += (f32x4){bflo(y.z), bfhi(y.z), bflo(y.w), bfhi(y.w)} * gt; } } }
.LBB0_3262:
	s_cmpk_gt_i32 s12, 0x3fff
	s_mov_b64 s[14:15], -1
	s_cbranch_scc1 .LBB0_3261
	v_or_b32_e32 v22, s22, v59
	ds_bpermute_b32 v24, v22, v68
	ds_bpermute_b32 v30, v22, v68 offset:4
	ds_bpermute_b32 v42, v22, v68 offset:12
	ds_bpermute_b32 v44, v22, v67
	ds_bpermute_b32 v46, v22, v67 offset:4
	s_waitcnt lgkmcnt(4)
	v_ashrrev_i32_e32 v25, 31, v24
	v_lshlrev_b64 v[24:25], 11, v[24:25]
	v_lshl_add_u64 v[24:25], v[2:3], 0, v[24:25]
	s_waitcnt lgkmcnt(3)
	v_ashrrev_i32_e32 v31, 31, v30
	global_load_dwordx2 v[26:27], v[24:25], off
	global_load_dwordx2 v[28:29], v[24:25], off offset:512
	global_load_dwordx2 v[32:33], v[24:25], off offset:1024
	global_load_dwordx2 v[34:35], v[24:25], off offset:1536
	v_lshlrev_b64 v[24:25], 11, v[30:31]
	v_lshl_add_u64 v[24:25], v[2:3], 0, v[24:25]
	global_load_dwordx2 v[30:31], v[24:25], off
	global_load_dwordx2 v[36:37], v[24:25], off offset:512
	global_load_dwordx2 v[38:39], v[24:25], off offset:1024
	global_load_dwordx2 v[40:41], v[24:25], off offset:1536
	ds_bpermute_b32 v24, v22, v68 offset:8
	s_waitcnt lgkmcnt(3)
	v_ashrrev_i32_e32 v43, 31, v42
	v_lshlrev_b64 v[42:43], 11, v[42:43]
	v_lshl_add_u64 v[42:43], v[2:3], 0, v[42:43]
	v_mov_b32_e32 v23, s19
	s_waitcnt lgkmcnt(0)
	v_ashrrev_i32_e32 v25, 31, v24
	v_lshlrev_b64 v[24:25], 11, v[24:25]
	v_lshl_add_u64 v[24:25], v[2:3], 0, v[24:25]
	global_load_dwordx2 v[48:49], v[24:25], off
	global_load_dwordx2 v[50:51], v[24:25], off offset:512
	global_load_dwordx2 v[52:53], v[24:25], off offset:1024
	global_load_dwordx2 v[70:71], v[24:25], off offset:1536
	global_load_dwordx2 v[72:73], v[42:43], off
	global_load_dwordx2 v[74:75], v[42:43], off offset:512
	global_load_dwordx2 v[76:77], v[42:43], off offset:1024
	global_load_dwordx2 v[78:79], v[42:43], off offset:1536
	s_ashr_i32 s13, s12, 31
	s_lshl_b64 s[14:15], s[12:13], 11
	v_or_b32_e32 v69, 28, v22
	v_cmp_lt_i32_e32 vcc, v61, v60
	s_waitcnt vmcnt(15)
	v_cvt_pk_f32_fp8_e32 v[24:25], v26
	s_waitcnt vmcnt(14)
	v_cvt_pk_f32_fp8_e32 v[82:83], v28
	v_cvt_pk_f32_fp8_sdwa v[84:85], v28 src0_sel:WORD_1
	v_cvt_pk_f32_fp8_e32 v[86:87], v29
	v_cvt_pk_f32_fp8_sdwa v[28:29], v29 src0_sel:WORD_1
	s_waitcnt vmcnt(10)
	v_cvt_pk_f32_fp8_e32 v[106:107], v36
	v_cvt_pk_f32_fp8_sdwa v[108:109], v36 src0_sel:WORD_1
	v_cvt_pk_f32_fp8_e32 v[110:111], v37
	v_cvt_pk_f32_fp8_sdwa v[36:37], v37 src0_sel:WORD_1
	v_cvt_pk_f32_fp8_sdwa v[42:43], v26 src0_sel:WORD_1
	v_cvt_pk_f32_fp8_e32 v[80:81], v27
	v_cvt_pk_f32_fp8_sdwa v[26:27], v27 src0_sel:WORD_1
	v_cvt_pk_f32_fp8_e32 v[88:89], v32
	v_cvt_pk_f32_fp8_sdwa v[90:91], v32 src0_sel:WORD_1
	v_cvt_pk_f32_fp8_e32 v[92:93], v33
	v_cvt_pk_f32_fp8_sdwa v[32:33], v33 src0_sel:WORD_1
	v_cvt_pk_f32_fp8_e32 v[94:95], v34
	v_cvt_pk_f32_fp8_sdwa v[96:97], v34 src0_sel:WORD_1
	v_cvt_pk_f32_fp8_e32 v[98:99], v35
	v_cvt_pk_f32_fp8_sdwa v[34:35], v35 src0_sel:WORD_1
	v_pk_fma_f32 v[86:87], v[44:45], v[86:87], 0 op_sel_hi:[0,1,0]
	v_pk_fma_f32 v[28:29], v[44:45], v[28:29], 0 op_sel_hi:[0,1,0]
	v_cvt_pk_f32_fp8_e32 v[100:101], v30
	v_cvt_pk_f32_fp8_sdwa v[102:103], v30 src0_sel:WORD_1
	v_cvt_pk_f32_fp8_e32 v[104:105], v31
	v_cvt_pk_f32_fp8_sdwa v[30:31], v31 src0_sel:WORD_1
	s_waitcnt vmcnt(9)
	v_cvt_pk_f32_fp8_e32 v[112:113], v38
	v_cvt_pk_f32_fp8_sdwa v[114:115], v38 src0_sel:WORD_1
	v_cvt_pk_f32_fp8_e32 v[116:117], v39
	v_cvt_pk_f32_fp8_sdwa v[38:39], v39 src0_sel:WORD_1
	s_waitcnt vmcnt(8)
	v_cvt_pk_f32_fp8_e32 v[118:119], v40
	v_cvt_pk_f32_fp8_sdwa v[120:121], v40 src0_sel:WORD_1
	v_cvt_pk_f32_fp8_sdwa v[122:123], v41 src0_sel:WORD_1
	v_pk_fma_f32 v[28:29], v[46:47], v[36:37], v[28:29] op_sel_hi:[0,1,1]
	v_pk_fma_f32 v[36:37], v[46:47], v[110:111], v[86:87] op_sel_hi:[0,1,1]
	v_cvt_pk_f32_fp8_e32 v[86:87], v41
	v_pk_fma_f32 v[24:25], v[44:45], v[24:25], 0 op_sel_hi:[0,1,0]
	v_pk_fma_f32 v[42:43], v[44:45], v[42:43], 0 op_sel_hi:[0,1,0]
	v_pk_fma_f32 v[80:81], v[44:45], v[80:81], 0 op_sel_hi:[0,1,0]
	v_pk_fma_f32 v[26:27], v[44:45], v[26:27], 0 op_sel_hi:[0,1,0]
	v_pk_fma_f32 v[82:83], v[44:45], v[82:83], 0 op_sel_hi:[0,1,0]
	v_pk_fma_f32 v[84:85], v[44:45], v[84:85], 0 op_sel_hi:[0,1,0]
	v_pk_fma_f32 v[88:89], v[44:45], v[88:89], 0 op_sel_hi:[0,1,0]
	v_pk_fma_f32 v[90:91], v[44:45], v[90:91], 0 op_sel_hi:[0,1,0]
	v_pk_fma_f32 v[92:93], v[44:45], v[92:93], 0 op_sel_hi:[0,1,0]
	v_pk_fma_f32 v[32:33], v[44:45], v[32:33], 0 op_sel_hi:[0,1,0]
	v_pk_fma_f32 v[94:95], v[44:45], v[94:95], 0 op_sel_hi:[0,1,0]
	v_pk_fma_f32 v[96:97], v[44:45], v[96:97], 0 op_sel_hi:[0,1,0]
	v_pk_fma_f32 v[98:99], v[44:45], v[98:99], 0 op_sel_hi:[0,1,0]
	v_pk_fma_f32 v[34:35], v[44:45], v[34:35], 0 op_sel_hi:[0,1,0]
	v_pk_fma_f32 v[42:43], v[46:47], v[102:103], v[42:43] op_sel_hi:[0,1,1]
	v_pk_fma_f32 v[24:25], v[46:47], v[100:101], v[24:25] op_sel_hi:[0,1,1]
	v_pk_fma_f32 v[26:27], v[46:47], v[30:31], v[26:27] op_sel_hi:[0,1,1]
	v_pk_fma_f32 v[30:31], v[46:47], v[104:105], v[80:81] op_sel_hi:[0,1,1]
	v_pk_fma_f32 v[44:45], v[46:47], v[108:109], v[84:85] op_sel_hi:[0,1,1]
	v_pk_fma_f32 v[80:81], v[46:47], v[106:107], v[82:83] op_sel_hi:[0,1,1]
	v_pk_fma_f32 v[82:83], v[46:47], v[114:115], v[90:91] op_sel_hi:[0,1,1]
	v_pk_fma_f32 v[84:85], v[46:47], v[112:113], v[88:89] op_sel_hi:[0,1,1]
	v_pk_fma_f32 v[32:33], v[46:47], v[38:39], v[32:33] op_sel_hi:[0,1,1]
	v_pk_fma_f32 v[38:39], v[46:47], v[116:117], v[92:93] op_sel_hi:[0,1,1]
	v_pk_fma_f32 v[88:89], v[46:47], v[120:121], v[96:97] op_sel_hi:[0,1,1]
	v_pk_fma_f32 v[90:91], v[46:47], v[118:119], v[94:95] op_sel_hi:[0,1,1]
	v_pk_fma_f32 v[34:35], v[46:47], v[122:123], v[34:35] op_sel_hi:[0,1,1]
	v_pk_fma_f32 v[46:47], v[46:47], v[86:87], v[98:99] op_sel_hi:[0,1,1]
	ds_bpermute_b32 v86, v22, v67 offset:8
	s_waitcnt vmcnt(7)
; #define GAS __attribute__((address_space(1)))
; template <bool Y8, bool LAST>
; __device__ __forceinline__ void combine_ln2_phase(Frame& F, int layer) {
;     ...
;         for (int k = 0; k < 9; ++k) { size_t row; float gt;
;             if (k < 8) { row = (size_t)__shfl(myrow, tj * 8 + k); gt = __shfl(mygate, tj * 8 + k); }
;             else { row = (size_t)toff[N_EXPERTS] * 256 + t; gt = 1.0f; }
;             if constexpr (Y8) {
;                 const GAS u32x2* yp = (const GAS u32x2*)((const GAS unsigned char*)Y + row * D_MODEL) + lane;
; #pragma unroll
;                 for (int j = 0; j < 4; ++j) { const u32x2 y = yp[64 * j];
;                     const f32x2 p0 = __builtin_amdgcn_cvt_pk_f32_fp8((int)y.x, false), p1 = __builtin_amdgcn_cvt_pk_f32_fp8((int)y.x, true), p2 = __builtin_amdgcn_cvt_pk_f32_fp8((int)y.y, false), p3 = __builtin_amdgcn_cvt_pk_f32_fp8((int)y.y, true);
;                     a[j][0] += (f32x4){p0[0], p0[1], p1[0], p1[1]} * gt; a[j][1] += (f32x4){p2[0], p2[1], p3[0], p3[1]} * gt; }
;             } else {
;             const GAS u32x4* yp = (const GAS u32x4*)(Y + row * D_MODEL) + lane;
; #pragma unroll
;             for (int j = 0; j < 4; ++j) { const u32x4 y = yp[64 * j];
;                 a[j][0] += (f32x4){bflo(y.x), bfhi(y.x), bflo(y.y), bfhi(y.y)} * gt; a[j][1] += (f32x4){bflo(y.z), bfhi(y.z), bflo(y.w), bfhi(y.w)} * gt; } } }
	v_cvt_pk_f32_fp8_e32 v[94:95], v48
	v_cvt_pk_f32_fp8_sdwa v[96:97], v48 src0_sel:WORD_1
	v_cvt_pk_f32_fp8_e32 v[98:99], v49
	v_cvt_pk_f32_fp8_sdwa v[48:49], v49 src0_sel:WORD_1
	ds_bpermute_b32 v40, v22, v68 offset:16
	s_waitcnt lgkmcnt(1)
	v_pk_fma_f32 v[24:25], v[86:87], v[94:95], v[24:25] op_sel_hi:[0,1,1]
	v_pk_fma_f32 v[30:31], v[86:87], v[98:99], v[30:31] op_sel_hi:[0,1,1]
	v_pk_fma_f32 v[26:27], v[86:87], v[48:49], v[26:27] op_sel_hi:[0,1,1]
	s_waitcnt vmcnt(6)
	v_cvt_pk_f32_fp8_e32 v[48:49], v50
	v_cvt_pk_f32_fp8_sdwa v[94:95], v50 src0_sel:WORD_1
	v_cvt_pk_f32_fp8_e32 v[98:99], v51
	v_cvt_pk_f32_fp8_sdwa v[50:51], v51 src0_sel:WORD_1
	v_pk_fma_f32 v[48:49], v[86:87], v[48:49], v[80:81] op_sel_hi:[0,1,1]
	s_waitcnt vmcnt(5)
	v_cvt_pk_f32_fp8_sdwa v[80:81], v52 src0_sel:WORD_1
	v_pk_fma_f32 v[36:37], v[86:87], v[98:99], v[36:37] op_sel_hi:[0,1,1]
	v_pk_fma_f32 v[28:29], v[86:87], v[50:51], v[28:29] op_sel_hi:[0,1,1]
	v_cvt_pk_f32_fp8_e32 v[50:51], v52
	v_cvt_pk_f32_fp8_e32 v[98:99], v53
	v_cvt_pk_f32_fp8_sdwa v[52:53], v53 src0_sel:WORD_1
	s_waitcnt lgkmcnt(0)
	v_ashrrev_i32_e32 v41, 31, v40
	v_lshlrev_b64 v[40:41], 11, v[40:41]
	v_lshl_add_u64 v[40:41], v[2:3], 0, v[40:41]
	global_load_dwordx2 v[92:93], v[40:41], off
	v_pk_fma_f32 v[32:33], v[86:87], v[52:53], v[32:33] op_sel_hi:[0,1,1]
	s_waitcnt vmcnt(5)
	v_cvt_pk_f32_fp8_e32 v[52:53], v70
	v_pk_fma_f32 v[42:43], v[86:87], v[96:97], v[42:43] op_sel_hi:[0,1,1]
	global_load_dwordx2 v[96:97], v[40:41], off offset:512
	v_pk_fma_f32 v[50:51], v[86:87], v[50:51], v[84:85] op_sel_hi:[0,1,1]
	v_pk_fma_f32 v[52:53], v[86:87], v[52:53], v[90:91] op_sel_hi:[0,1,1]
	ds_bpermute_b32 v90, v22, v68 offset:20
	v_cvt_pk_f32_fp8_e32 v[84:85], v71
	v_pk_fma_f32 v[44:45], v[86:87], v[94:95], v[44:45] op_sel_hi:[0,1,1]
	global_load_dwordx2 v[94:95], v[40:41], off offset:1024
	v_pk_fma_f32 v[80:81], v[86:87], v[80:81], v[82:83] op_sel_hi:[0,1,1]
	v_cvt_pk_f32_fp8_sdwa v[82:83], v70 src0_sel:WORD_1
	v_cvt_pk_f32_fp8_sdwa v[70:71], v71 src0_sel:WORD_1
	s_waitcnt lgkmcnt(0)
	v_ashrrev_i32_e32 v91, 31, v90
	v_pk_fma_f32 v[46:47], v[86:87], v[84:85], v[46:47] op_sel_hi:[0,1,1]
	v_lshlrev_b64 v[84:85], 11, v[90:91]
	v_lshl_add_u64 v[84:85], v[2:3], 0, v[84:85]
	v_pk_fma_f32 v[38:39], v[86:87], v[98:99], v[38:39] op_sel_hi:[0,1,1]
	v_pk_fma_f32 v[82:83], v[86:87], v[82:83], v[88:89] op_sel_hi:[0,1,1]
	v_pk_fma_f32 v[34:35], v[86:87], v[70:71], v[34:35] op_sel_hi:[0,1,1]
	global_load_dwordx2 v[86:87], v[84:85], off
	ds_bpermute_b32 v70, v22, v67 offset:12
	global_load_dwordx2 v[40:41], v[40:41], off offset:1536
	s_waitcnt vmcnt(8)
	v_cvt_pk_f32_fp8_e32 v[90:91], v72
	v_cvt_pk_f32_fp8_sdwa v[98:99], v73 src0_sel:WORD_1
	v_cvt_pk_f32_fp8_sdwa v[88:89], v72 src0_sel:WORD_1
	v_cvt_pk_f32_fp8_e32 v[72:73], v73
	s_waitcnt lgkmcnt(0)
	v_pk_fma_f32 v[24:25], v[70:71], v[90:91], v[24:25] op_sel_hi:[0,1,1]
	v_pk_fma_f32 v[26:27], v[70:71], v[98:99], v[26:27] op_sel_hi:[0,1,1]
	s_waitcnt vmcnt(7)
	v_cvt_pk_f32_fp8_sdwa v[90:91], v75 src0_sel:WORD_1
	global_load_dwordx2 v[98:99], v[84:85], off offset:512
	v_pk_fma_f32 v[42:43], v[70:71], v[88:89], v[42:43] op_sel_hi:[0,1,1]
	v_pk_fma_f32 v[30:31], v[70:71], v[72:73], v[30:31] op_sel_hi:[0,1,1]
	v_cvt_pk_f32_fp8_e32 v[72:73], v74
	v_cvt_pk_f32_fp8_sdwa v[88:89], v74 src0_sel:WORD_1
	v_cvt_pk_f32_fp8_e32 v[74:75], v75
	v_pk_fma_f32 v[28:29], v[70:71], v[90:91], v[28:29] op_sel_hi:[0,1,1]
	global_load_dwordx2 v[90:91], v[84:85], off offset:1024
	v_pk_fma_f32 v[44:45], v[70:71], v[88:89], v[44:45] op_sel_hi:[0,1,1]
	v_pk_fma_f32 v[48:49], v[70:71], v[72:73], v[48:49] op_sel_hi:[0,1,1]
	v_pk_fma_f32 v[36:37], v[70:71], v[74:75], v[36:37] op_sel_hi:[0,1,1]
	s_waitcnt vmcnt(8)
	v_cvt_pk_f32_fp8_e32 v[72:73], v76
	v_cvt_pk_f32_fp8_sdwa v[74:75], v76 src0_sel:WORD_1
	v_cvt_pk_f32_fp8_sdwa v[88:89], v77 src0_sel:WORD_1
	v_cvt_pk_f32_fp8_e32 v[76:77], v77
	v_pk_fma_f32 v[50:51], v[70:71], v[72:73], v[50:51] op_sel_hi:[0,1,1]
	v_pk_fma_f32 v[74:75], v[70:71], v[74:75], v[80:81] op_sel_hi:[0,1,1]
	s_waitcnt vmcnt(7)
	v_cvt_pk_f32_fp8_sdwa v[72:73], v78 src0_sel:WORD_1
	v_pk_fma_f32 v[38:39], v[70:71], v[76:77], v[38:39] op_sel_hi:[0,1,1]
	v_cvt_pk_f32_fp8_e32 v[76:77], v78
	v_cvt_pk_f32_fp8_e32 v[80:81], v79
	v_cvt_pk_f32_fp8_sdwa v[78:79], v79 src0_sel:WORD_1
	v_pk_fma_f32 v[32:33], v[70:71], v[88:89], v[32:33] op_sel_hi:[0,1,1]
	v_pk_fma_f32 v[52:53], v[70:71], v[76:77], v[52:53] op_sel_hi:[0,1,1]
	global_load_dwordx2 v[76:77], v[84:85], off offset:1536
	ds_bpermute_b32 v84, v22, v68 offset:24
	v_pk_fma_f32 v[72:73], v[70:71], v[72:73], v[82:83] op_sel_hi:[0,1,1]
	v_pk_fma_f32 v[34:35], v[70:71], v[78:79], v[34:35] op_sel_hi:[0,1,1]
	v_pk_fma_f32 v[46:47], v[70:71], v[80:81], v[46:47] op_sel_hi:[0,1,1]
	ds_bpermute_b32 v70, v22, v67 offset:16
	s_waitcnt lgkmcnt(1)
	v_ashrrev_i32_e32 v85, 31, v84
	s_waitcnt vmcnt(7)
	v_cvt_pk_f32_fp8_e32 v[78:79], v92
	v_cvt_pk_f32_fp8_sdwa v[88:89], v93 src0_sel:WORD_1
	v_cvt_pk_f32_fp8_sdwa v[80:81], v92 src0_sel:WORD_1
	v_cvt_pk_f32_fp8_e32 v[82:83], v93
	s_waitcnt lgkmcnt(0)
	v_pk_fma_f32 v[24:25], v[70:71], v[78:79], v[24:25] op_sel_hi:[0,1,1]
	v_lshlrev_b64 v[78:79], 11, v[84:85]
	v_pk_fma_f32 v[26:27], v[70:71], v[88:89], v[26:27] op_sel_hi:[0,1,1]
	s_waitcnt vmcnt(6)
	v_cvt_pk_f32_fp8_sdwa v[84:85], v96 src0_sel:WORD_1
	v_cvt_pk_f32_fp8_e32 v[88:89], v97
	v_cvt_pk_f32_fp8_sdwa v[92:93], v97 src0_sel:WORD_1
	v_pk_fma_f32 v[30:31], v[70:71], v[82:83], v[30:31] op_sel_hi:[0,1,1]
	v_cvt_pk_f32_fp8_e32 v[82:83], v96
	v_pk_fma_f32 v[44:45], v[70:71], v[84:85], v[44:45] op_sel_hi:[0,1,1]
	v_pk_fma_f32 v[36:37], v[70:71], v[88:89], v[36:37] op_sel_hi:[0,1,1]
	v_pk_fma_f32 v[28:29], v[70:71], v[92:93], v[28:29] op_sel_hi:[0,1,1]
	s_waitcnt vmcnt(5)
; #define GAS __attribute__((address_space(1)))
; template <bool Y8, bool LAST>
; __device__ __forceinline__ void combine_ln2_phase(Frame& F, int layer) {
;     ...
;         for (int k = 0; k < 9; ++k) { size_t row; float gt;
;             if (k < 8) { row = (size_t)__shfl(myrow, tj * 8 + k); gt = __shfl(mygate, tj * 8 + k); }
;             else { row = (size_t)toff[N_EXPERTS] * 256 + t; gt = 1.0f; }
;             if constexpr (Y8) {
;                 const GAS u32x2* yp = (const GAS u32x2*)((const GAS unsigned char*)Y + row * D_MODEL) + lane;
; #pragma unroll
;                 for (int j = 0; j < 4; ++j) { const u32x2 y = yp[64 * j];
;                     const f32x2 p0 = __builtin_amdgcn_cvt_pk_f32_fp8((int)y.x, false), p1 = __builtin_amdgcn_cvt_pk_f32_fp8((int)y.x, true), p2 = __builtin_amdgcn_cvt_pk_f32_fp8((int)y.y, false), p3 = __builtin_amdgcn_cvt_pk_f32_fp8((int)y.y, true);
;                     a[j][0] += (f32x4){p0[0], p0[1], p1[0], p1[1]} * gt; a[j][1] += (f32x4){p2[0], p2[1], p3[0], p3[1]} * gt; }
;             } else {
;             const GAS u32x4* yp = (const GAS u32x4*)(Y + row * D_MODEL) + lane;
; #pragma unroll
;             for (int j = 0; j < 4; ++j) { const u32x4 y = yp[64 * j];
;                 a[j][0] += (f32x4){bflo(y.x), bfhi(y.x), bflo(y.y), bfhi(y.y)} * gt; a[j][1] += (f32x4){bflo(y.z), bfhi(y.z), bflo(y.w), bfhi(y.w)} * gt; } } }
;         float s = 0.f;
; #pragma unroll
;         for (int j = 0; j < 4; ++j) { const u32x4 xv = *(const GAS u32x4*)(X1B + (size_t)t * D_MODEL + 8 * lane + 512 * j);
;             a[j][0] += (f32x4){bflo(xv.x), bfhi(xv.x), bflo(xv.y), bfhi(xv.y)} * DN_ALPHA; a[j][1] += (f32x4){bflo(xv.z), bfhi(xv.z), bflo(xv.w), bfhi(xv.w)} * DN_ALPHA;
;             s += (a[j][0][0] + a[j][0][1]) + (a[j][0][2] + a[j][0][3]) + (a[j][1][0] + a[j][1][1]) + (a[j][1][2] + a[j][1][3]); }
	v_cvt_pk_f32_fp8_e32 v[84:85], v94
	v_cvt_pk_f32_fp8_sdwa v[88:89], v94 src0_sel:WORD_1
	v_cvt_pk_f32_fp8_e32 v[92:93], v95
	v_cvt_pk_f32_fp8_sdwa v[94:95], v95 src0_sel:WORD_1
	v_lshl_add_u64 v[78:79], v[2:3], 0, v[78:79]
	v_pk_fma_f32 v[42:43], v[70:71], v[80:81], v[42:43] op_sel_hi:[0,1,1]
	global_load_dwordx2 v[80:81], v[78:79], off
	v_pk_fma_f32 v[48:49], v[70:71], v[82:83], v[48:49] op_sel_hi:[0,1,1]
	global_load_dwordx2 v[82:83], v[78:79], off offset:512
	v_pk_fma_f32 v[50:51], v[70:71], v[84:85], v[50:51] op_sel_hi:[0,1,1]
	v_pk_fma_f32 v[74:75], v[70:71], v[88:89], v[74:75] op_sel_hi:[0,1,1]
	v_pk_fma_f32 v[38:39], v[70:71], v[92:93], v[38:39] op_sel_hi:[0,1,1]
	v_pk_fma_f32 v[32:33], v[70:71], v[94:95], v[32:33] op_sel_hi:[0,1,1]
	global_load_dwordx2 v[84:85], v[78:79], off offset:1024
	s_waitcnt vmcnt(6)
	v_cvt_pk_f32_fp8_e32 v[88:89], v40
	v_cvt_pk_f32_fp8_sdwa v[92:93], v40 src0_sel:WORD_1
	v_cvt_pk_f32_fp8_e32 v[94:95], v41
	v_cvt_pk_f32_fp8_sdwa v[40:41], v41 src0_sel:WORD_1
	v_pk_fma_f32 v[52:53], v[70:71], v[88:89], v[52:53] op_sel_hi:[0,1,1]
	v_pk_fma_f32 v[72:73], v[70:71], v[92:93], v[72:73] op_sel_hi:[0,1,1]
	v_pk_fma_f32 v[46:47], v[70:71], v[94:95], v[46:47] op_sel_hi:[0,1,1]
	v_pk_fma_f32 v[34:35], v[70:71], v[40:41], v[34:35] op_sel_hi:[0,1,1]
	ds_bpermute_b32 v40, v22, v67 offset:20
	v_cvt_pk_f32_fp8_e32 v[88:89], v86
	v_cvt_pk_f32_fp8_sdwa v[92:93], v86 src0_sel:WORD_1
	v_cvt_pk_f32_fp8_e32 v[94:95], v87
	v_cvt_pk_f32_fp8_sdwa v[86:87], v87 src0_sel:WORD_1
	s_waitcnt lgkmcnt(0)
	v_pk_fma_f32 v[24:25], v[40:41], v[88:89], v[24:25] op_sel_hi:[0,1,1]
	v_pk_fma_f32 v[42:43], v[40:41], v[92:93], v[42:43] op_sel_hi:[0,1,1]
	s_waitcnt vmcnt(5)
	v_cvt_pk_f32_fp8_sdwa v[88:89], v98 src0_sel:WORD_1
	v_pk_fma_f32 v[26:27], v[40:41], v[86:87], v[26:27] op_sel_hi:[0,1,1]
	v_cvt_pk_f32_fp8_e32 v[86:87], v98
	v_cvt_pk_f32_fp8_sdwa v[92:93], v99 src0_sel:WORD_1
	v_pk_fma_f32 v[44:45], v[40:41], v[88:89], v[44:45] op_sel_hi:[0,1,1]
	s_waitcnt vmcnt(4)
	v_cvt_pk_f32_fp8_sdwa v[88:89], v90 src0_sel:WORD_1
	v_pk_fma_f32 v[48:49], v[40:41], v[86:87], v[48:49] op_sel_hi:[0,1,1]
	v_cvt_pk_f32_fp8_e32 v[86:87], v90
	v_pk_fma_f32 v[28:29], v[40:41], v[92:93], v[28:29] op_sel_hi:[0,1,1]
	v_cvt_pk_f32_fp8_sdwa v[92:93], v91 src0_sel:WORD_1
	v_cvt_pk_f32_fp8_e32 v[90:91], v91
	v_pk_fma_f32 v[50:51], v[40:41], v[86:87], v[50:51] op_sel_hi:[0,1,1]
	ds_read_b32 v86, v23
	v_cvt_pk_f32_fp8_e32 v[98:99], v99
	v_pk_fma_f32 v[74:75], v[40:41], v[88:89], v[74:75] op_sel_hi:[0,1,1]
	v_pk_fma_f32 v[38:39], v[40:41], v[90:91], v[38:39] op_sel_hi:[0,1,1]
	s_waitcnt vmcnt(3)
	v_cvt_pk_f32_fp8_e32 v[88:89], v76
	v_cvt_pk_f32_fp8_sdwa v[90:91], v76 src0_sel:WORD_1
	s_waitcnt lgkmcnt(0)
	v_ashrrev_i32_e32 v87, 31, v86
	v_cvt_pk_f32_fp8_sdwa v[100:101], v77 src0_sel:WORD_1
	v_cvt_pk_f32_fp8_e32 v[76:77], v77
	v_lshlrev_b64 v[86:87], 19, v[86:87]
	v_lshl_add_u64 v[86:87], v[2:3], 0, v[86:87]
	v_lshl_add_u64 v[86:87], v[86:87], 0, s[14:15]
	global_load_dwordx2 v[70:71], v[78:79], off offset:1536
	v_pk_fma_f32 v[30:31], v[40:41], v[94:95], v[30:31] op_sel_hi:[0,1,1]
	v_pk_fma_f32 v[36:37], v[40:41], v[98:99], v[36:37] op_sel_hi:[0,1,1]
	v_pk_fma_f32 v[32:33], v[40:41], v[92:93], v[32:33] op_sel_hi:[0,1,1]
	v_pk_fma_f32 v[72:73], v[40:41], v[90:91], v[72:73] op_sel_hi:[0,1,1]
	v_pk_fma_f32 v[52:53], v[40:41], v[88:89], v[52:53] op_sel_hi:[0,1,1]
	v_pk_fma_f32 v[34:35], v[40:41], v[100:101], v[34:35] op_sel_hi:[0,1,1]
	v_pk_fma_f32 v[40:41], v[40:41], v[76:77], v[46:47] op_sel_hi:[0,1,1]
	global_load_dwordx2 v[76:77], v[86:87], off offset:512
	ds_bpermute_b32 v78, v69, v68
	global_load_dwordx2 v[92:93], v[86:87], off
	ds_bpermute_b32 v46, v22, v67 offset:24
	s_lshl_b64 s[14:15], s[12:13], 12
	s_waitcnt lgkmcnt(1)
	v_ashrrev_i32_e32 v79, 31, v78
	v_lshlrev_b64 v[78:79], 11, v[78:79]
	v_lshl_add_u64 v[78:79], v[2:3], 0, v[78:79]
	global_load_dwordx2 v[96:97], v[78:79], off
	global_load_dwordx2 v[94:95], v[78:79], off offset:512
	global_load_dwordx2 v[98:99], v[78:79], off offset:1024
	s_waitcnt vmcnt(8)
	v_cvt_pk_f32_fp8_e32 v[22:23], v80
	global_load_dwordx2 v[78:79], v[78:79], off offset:1536
	v_cvt_pk_f32_fp8_sdwa v[88:89], v80 src0_sel:WORD_1
	v_cvt_pk_f32_fp8_e32 v[90:91], v81
	s_waitcnt lgkmcnt(0)
	v_pk_fma_f32 v[100:101], v[46:47], v[22:23], v[24:25] op_sel_hi:[0,1,1]
	s_waitcnt vmcnt(8)
	v_cvt_pk_f32_fp8_e32 v[22:23], v82
	v_pk_fma_f32 v[42:43], v[46:47], v[88:89], v[42:43] op_sel_hi:[0,1,1]
	v_cvt_pk_f32_fp8_sdwa v[24:25], v82 src0_sel:WORD_1
	v_cvt_pk_f32_fp8_e32 v[88:89], v83
	v_cvt_pk_f32_fp8_sdwa v[82:83], v83 src0_sel:WORD_1
	v_pk_fma_f32 v[48:49], v[46:47], v[22:23], v[48:49] op_sel_hi:[0,1,1]
	s_waitcnt vmcnt(7)
	v_cvt_pk_f32_fp8_e32 v[22:23], v84
	v_pk_fma_f32 v[36:37], v[46:47], v[88:89], v[36:37] op_sel_hi:[0,1,1]
	v_pk_fma_f32 v[82:83], v[46:47], v[82:83], v[28:29] op_sel_hi:[0,1,1]
	v_cvt_pk_f32_fp8_sdwa v[28:29], v84 src0_sel:WORD_1
	v_cvt_pk_f32_fp8_e32 v[88:89], v85
	v_cvt_pk_f32_fp8_sdwa v[84:85], v85 src0_sel:WORD_1
	v_cvt_pk_f32_fp8_sdwa v[80:81], v81 src0_sel:WORD_1
	v_pk_fma_f32 v[74:75], v[46:47], v[28:29], v[74:75] op_sel_hi:[0,1,1]
	v_pk_fma_f32 v[38:39], v[46:47], v[88:89], v[38:39] op_sel_hi:[0,1,1]
	v_pk_fma_f32 v[32:33], v[46:47], v[84:85], v[32:33] op_sel_hi:[0,1,1]
	v_pk_fma_f32 v[30:31], v[46:47], v[90:91], v[30:31] op_sel_hi:[0,1,1]
	v_pk_fma_f32 v[26:27], v[46:47], v[80:81], v[26:27] op_sel_hi:[0,1,1]
	v_pk_fma_f32 v[44:45], v[46:47], v[24:25], v[44:45] op_sel_hi:[0,1,1]
	v_pk_fma_f32 v[50:51], v[46:47], v[22:23], v[50:51] op_sel_hi:[0,1,1]
	global_load_dwordx2 v[80:81], v[86:87], off offset:1024
	v_lshl_add_u64 v[90:91], v[4:5], 0, s[14:15]
	global_load_dwordx2 v[86:87], v[86:87], off offset:1536
	s_lshl_b64 s[14:15], s[12:13], 13
	global_load_dwordx4 v[22:25], v[90:91], off
	s_add_u32 s14, s2, s14
	s_addc_u32 s15, s3, s15
	s_add_i32 s22, s22, 32
	s_add_i32 s12, s12, s18
	s_cmpk_eq_i32 s22, 0x100
	s_waitcnt vmcnt(9)
; #define GAS __attribute__((address_space(1)))
; template <bool Y8, bool LAST>
; __device__ __forceinline__ void combine_ln2_phase(Frame& F, int layer) {
;     ...
;         for (int k = 0; k < 9; ++k) { size_t row; float gt;
;             if (k < 8) { row = (size_t)__shfl(myrow, tj * 8 + k); gt = __shfl(mygate, tj * 8 + k); }
;             else { row = (size_t)toff[N_EXPERTS] * 256 + t; gt = 1.0f; }
;             if constexpr (Y8) {
;                 const GAS u32x2* yp = (const GAS u32x2*)((const GAS unsigned char*)Y + row * D_MODEL) + lane;
; #pragma unroll
;                 for (int j = 0; j < 4; ++j) { const u32x2 y = yp[64 * j];
;                     const f32x2 p0 = __builtin_amdgcn_cvt_pk_f32_fp8((int)y.x, false), p1 = __builtin_amdgcn_cvt_pk_f32_fp8((int)y.x, true), p2 = __builtin_amdgcn_cvt_pk_f32_fp8((int)y.y, false), p3 = __builtin_amdgcn_cvt_pk_f32_fp8((int)y.y, true);
;                     a[j][0] += (f32x4){p0[0], p0[1], p1[0], p1[1]} * gt; a[j][1] += (f32x4){p2[0], p2[1], p3[0], p3[1]} * gt; }
;             } else {
;             const GAS u32x4* yp = (const GAS u32x4*)(Y + row * D_MODEL) + lane;
; #pragma unroll
;             for (int j = 0; j < 4; ++j) { const u32x4 y = yp[64 * j];
;                 a[j][0] += (f32x4){bflo(y.x), bfhi(y.x), bflo(y.y), bfhi(y.y)} * gt; a[j][1] += (f32x4){bflo(y.z), bfhi(y.z), bflo(y.w), bfhi(y.w)} * gt; } } }
;         float s = 0.f;
; #pragma unroll
;         for (int j = 0; j < 4; ++j) { const u32x4 xv = *(const GAS u32x4*)(X1B + (size_t)t * D_MODEL + 8 * lane + 512 * j);
;             a[j][0] += (f32x4){bflo(xv.x), bfhi(xv.x), bflo(xv.y), bfhi(xv.y)} * DN_ALPHA; a[j][1] += (f32x4){bflo(xv.z), bfhi(xv.z), bflo(xv.w), bfhi(xv.w)} * DN_ALPHA;
;             s += (a[j][0][0] + a[j][0][1]) + (a[j][0][2] + a[j][0][3]) + (a[j][1][0] + a[j][1][1]) + (a[j][1][2] + a[j][1][3]); }
	v_cvt_pk_f32_fp8_e32 v[28:29], v70
	v_cvt_pk_f32_fp8_sdwa v[84:85], v70 src0_sel:WORD_1
	v_cvt_pk_f32_fp8_e32 v[88:89], v71
	v_cvt_pk_f32_fp8_sdwa v[70:71], v71 src0_sel:WORD_1
	v_pk_fma_f32 v[52:53], v[46:47], v[28:29], v[52:53] op_sel_hi:[0,1,1]
	v_pk_fma_f32 v[72:73], v[46:47], v[84:85], v[72:73] op_sel_hi:[0,1,1]
	v_pk_fma_f32 v[40:41], v[46:47], v[88:89], v[40:41] op_sel_hi:[0,1,1]
	v_pk_fma_f32 v[34:35], v[46:47], v[70:71], v[34:35] op_sel_hi:[0,1,1]
	ds_bpermute_b32 v46, v69, v67
	s_waitcnt vmcnt(6)
	v_cvt_pk_f32_fp8_e32 v[70:71], v96
	v_cvt_pk_f32_fp8_e32 v[88:89], v97
	v_cvt_pk_f32_fp8_sdwa v[28:29], v96 src0_sel:WORD_1
	v_cvt_pk_f32_fp8_sdwa v[84:85], v97 src0_sel:WORD_1
	s_waitcnt lgkmcnt(0)
	v_pk_fma_f32 v[70:71], v[46:47], v[70:71], v[100:101] op_sel_hi:[0,1,1]
	v_pk_fma_f32 v[88:89], v[46:47], v[88:89], v[30:31] op_sel_hi:[0,1,1]
	s_waitcnt vmcnt(5)
	v_cvt_pk_f32_fp8_e32 v[30:31], v94
	v_cvt_pk_f32_fp8_sdwa v[96:97], v94 src0_sel:WORD_1
	v_cvt_pk_f32_fp8_e32 v[100:101], v95
	v_cvt_pk_f32_fp8_sdwa v[94:95], v95 src0_sel:WORD_1
	v_pk_fma_f32 v[48:49], v[46:47], v[30:31], v[48:49] op_sel_hi:[0,1,1]
	v_pk_fma_f32 v[44:45], v[46:47], v[96:97], v[44:45] op_sel_hi:[0,1,1]
	s_waitcnt vmcnt(4)
	v_cvt_pk_f32_fp8_sdwa v[30:31], v98 src0_sel:WORD_1
	v_pk_fma_f32 v[82:83], v[46:47], v[94:95], v[82:83] op_sel_hi:[0,1,1]
	v_cvt_pk_f32_fp8_e32 v[94:95], v98
	v_cvt_pk_f32_fp8_sdwa v[96:97], v99 src0_sel:WORD_1
	v_cvt_pk_f32_fp8_e32 v[98:99], v99
	v_pk_fma_f32 v[74:75], v[46:47], v[30:31], v[74:75] op_sel_hi:[0,1,1]
	v_pk_fma_f32 v[50:51], v[46:47], v[94:95], v[50:51] op_sel_hi:[0,1,1]
	v_pk_fma_f32 v[94:95], v[46:47], v[96:97], v[32:33] op_sel_hi:[0,1,1]
	s_waitcnt vmcnt(3)
	v_cvt_pk_f32_fp8_sdwa v[30:31], v78 src0_sel:WORD_1
	v_cvt_pk_f32_fp8_e32 v[32:33], v78
	v_cvt_pk_f32_fp8_sdwa v[96:97], v79 src0_sel:WORD_1
	v_cvt_pk_f32_fp8_e32 v[78:79], v79
	v_pk_fma_f32 v[42:43], v[46:47], v[28:29], v[42:43] op_sel_hi:[0,1,1]
	v_pk_fma_f32 v[84:85], v[46:47], v[84:85], v[26:27] op_sel_hi:[0,1,1]
	global_load_dwordx4 v[26:29], v[90:91], off offset:1024
	v_pk_fma_f32 v[36:37], v[46:47], v[100:101], v[36:37] op_sel_hi:[0,1,1]
	v_pk_fma_f32 v[38:39], v[46:47], v[98:99], v[38:39] op_sel_hi:[0,1,1]
	v_pk_fma_f32 v[98:99], v[46:47], v[30:31], v[72:73] op_sel_hi:[0,1,1]
	v_pk_fma_f32 v[52:53], v[46:47], v[32:33], v[52:53] op_sel_hi:[0,1,1]
	v_pk_fma_f32 v[34:35], v[46:47], v[96:97], v[34:35] op_sel_hi:[0,1,1]
	v_pk_fma_f32 v[40:41], v[46:47], v[78:79], v[40:41] op_sel_hi:[0,1,1]
	v_cvt_pk_f32_fp8_e32 v[46:47], v92
	v_cvt_pk_f32_fp8_sdwa v[72:73], v92 src0_sel:WORD_1
	v_cvt_pk_f32_fp8_e32 v[78:79], v93
	v_cvt_pk_f32_fp8_sdwa v[92:93], v93 src0_sel:WORD_1
	v_pk_add_f32 v[46:47], v[70:71], v[46:47]
	v_pk_add_f32 v[42:43], v[42:43], v[72:73]
	v_cvt_pk_f32_fp8_e32 v[70:71], v76
	v_cvt_pk_f32_fp8_sdwa v[72:73], v76 src0_sel:WORD_1
	global_load_dwordx4 v[30:33], v[90:91], off offset:2048
	v_pk_add_f32 v[84:85], v[84:85], v[92:93]
	v_pk_add_f32 v[92:93], v[48:49], v[70:71]
	v_pk_add_f32 v[44:45], v[44:45], v[72:73]
	global_load_dwordx4 v[70:73], v[90:91], off offset:3072
	v_pk_add_f32 v[78:79], v[88:89], v[78:79]
	v_cvt_pk_f32_fp8_e32 v[88:89], v77
	v_cvt_pk_f32_fp8_sdwa v[76:77], v77 src0_sel:WORD_1
	s_waitcnt vmcnt(5)
	v_cvt_pk_f32_fp8_e32 v[48:49], v80
	v_pk_add_f32 v[36:37], v[36:37], v[88:89]
	v_pk_add_f32 v[76:77], v[82:83], v[76:77]
	v_cvt_pk_f32_fp8_sdwa v[82:83], v80 src0_sel:WORD_1
	v_cvt_pk_f32_fp8_e32 v[88:89], v81
	v_pk_add_f32 v[90:91], v[50:51], v[48:49]
	s_waitcnt vmcnt(4)
	v_cvt_pk_f32_fp8_sdwa v[48:49], v86 src0_sel:WORD_1
	v_pk_add_f32 v[74:75], v[74:75], v[82:83]
	v_pk_add_f32 v[82:83], v[38:39], v[88:89]
	v_cvt_pk_f32_fp8_e32 v[38:39], v86
	v_cvt_pk_f32_fp8_e32 v[50:51], v87
	v_cvt_pk_f32_fp8_sdwa v[86:87], v87 src0_sel:WORD_1
	v_cvt_pk_f32_fp8_sdwa v[80:81], v81 src0_sel:WORD_1
	v_pk_add_f32 v[88:89], v[52:53], v[38:39]
	v_pk_add_f32 v[96:97], v[40:41], v[50:51]
	v_pk_add_f32 v[86:87], v[34:35], v[86:87]
	s_waitcnt vmcnt(3)
	v_lshlrev_b32_e32 v34, 16, v22
	v_and_b32_e32 v35, 0xffff0000, v22
	v_lshlrev_b32_e32 v22, 16, v23
	v_and_b32_e32 v23, 0xffff0000, v23
	v_pk_fma_f32 v[50:51], v[22:23], s[10:11], v[42:43] op_sel_hi:[1,0,1]
	v_pk_fma_f32 v[52:53], v[34:35], s[10:11], v[46:47] op_sel_hi:[1,0,1]
	v_lshlrev_b32_e32 v22, 16, v24
	v_and_b32_e32 v23, 0xffff0000, v24
	v_lshlrev_b32_e32 v24, 16, v25
	v_and_b32_e32 v25, 0xffff0000, v25
	v_pk_add_f32 v[80:81], v[94:95], v[80:81]
	v_pk_add_f32 v[94:95], v[98:99], v[48:49]
	v_pk_fma_f32 v[46:47], v[24:25], s[10:11], v[84:85] op_sel_hi:[1,0,1]
	v_pk_fma_f32 v[48:49], v[22:23], s[10:11], v[78:79] op_sel_hi:[1,0,1]
	v_pk_mov_b32 v[22:23], v[52:53], v[50:51] op_sel:[1,0]
	v_mov_b32_e32 v24, v52
	v_mov_b32_e32 v25, v51
	v_pk_add_f32 v[22:23], v[22:23], v[24:25]
	v_mov_b32_e32 v24, v46
	v_mov_b32_e32 v25, v48
	v_mov_b32_e32 v34, v47
	v_mov_b32_e32 v35, v49
	v_pk_add_f32 v[24:25], v[24:25], v[34:35]
	v_add_f32_e32 v22, v22, v23
	v_add_f32_e32 v22, v25, v22
	v_add_f32_e32 v22, v24, v22
	v_add_f32_e32 v78, 0, v22
	s_waitcnt vmcnt(2)
	v_lshlrev_b32_e32 v22, 16, v26
	v_and_b32_e32 v23, 0xffff0000, v26
	v_lshlrev_b32_e32 v24, 16, v27
	v_and_b32_e32 v25, 0xffff0000, v27
	v_pk_fma_f32 v[44:45], v[24:25], s[10:11], v[44:45] op_sel_hi:[1,0,1]
	v_pk_fma_f32 v[42:43], v[22:23], s[10:11], v[92:93] op_sel_hi:[1,0,1]
	v_lshlrev_b32_e32 v22, 16, v28
	v_and_b32_e32 v23, 0xffff0000, v28
	v_lshlrev_b32_e32 v24, 16, v29
	v_and_b32_e32 v25, 0xffff0000, v29
	v_pk_fma_f32 v[40:41], v[24:25], s[10:11], v[76:77] op_sel_hi:[1,0,1]
	v_pk_fma_f32 v[38:39], v[22:23], s[10:11], v[36:37] op_sel_hi:[1,0,1]
	v_pk_mov_b32 v[22:23], v[42:43], v[44:45] op_sel:[1,0]
	v_mov_b32_e32 v24, v42
	v_mov_b32_e32 v25, v45
	v_pk_add_f32 v[22:23], v[22:23], v[24:25]
	v_mov_b32_e32 v24, v40
	v_mov_b32_e32 v25, v38
	v_mov_b32_e32 v26, v41
	v_mov_b32_e32 v27, v39
	v_pk_add_f32 v[22:23], v[22:23], v[22:23] op_sel:[0,1] op_sel_hi:[1,0]
	v_pk_add_f32 v[24:25], v[24:25], v[26:27]
	s_waitcnt vmcnt(0)
; #define GAS __attribute__((address_space(1)))
; template <bool Y8, bool LAST>
; __device__ __forceinline__ void combine_ln2_phase(Frame& F, int layer) {
;     ...
;         for (int j = 0; j < 4; ++j) { const u32x4 xv = *(const GAS u32x4*)(X1B + (size_t)t * D_MODEL + 8 * lane + 512 * j);
;             a[j][0] += (f32x4){bflo(xv.x), bfhi(xv.x), bflo(xv.y), bfhi(xv.y)} * DN_ALPHA; a[j][1] += (f32x4){bflo(xv.z), bfhi(xv.z), bflo(xv.w), bfhi(xv.w)} * DN_ALPHA;
;             s += (a[j][0][0] + a[j][0][1]) + (a[j][0][2] + a[j][0][3]) + (a[j][1][0] + a[j][1][1]) + (a[j][1][2] + a[j][1][3]); }
;         const float mean = wave_sum(s) * (1.0f / D_MODEL); float s2 = 0.f;
; #pragma unroll
;         for (int j = 0; j < 4; ++j) { a[j][0] = a[j][0] - mean; a[j][1] = a[j][1] - mean;
;             s2 += (a[j][0][0] * a[j][0][0] + a[j][0][1] * a[j][0][1]) + (a[j][0][2] * a[j][0][2] + a[j][0][3] * a[j][0][3]) + (a[j][1][0] * a[j][1][0] + a[j][1][1] * a[j][1][1]) + (a[j][1][2] * a[j][1][2] + a[j][1][3] * a[j][1][3]); }
;         const float rstd = rsqrtf(wave_sum(s2) * (1.0f / D_MODEL) + LN_EPS);
	v_lshlrev_b32_e32 v26, 16, v72
	v_pk_add_f32 v[22:23], v[24:25], v[22:23] op_sel:[1,0] op_sel_hi:[0,1]
	v_pk_add_f32 v[76:77], v[24:25], v[22:23]
	v_lshlrev_b32_e32 v22, 16, v30
	v_and_b32_e32 v23, 0xffff0000, v30
	v_lshlrev_b32_e32 v24, 16, v31
	v_and_b32_e32 v25, 0xffff0000, v31
	v_pk_fma_f32 v[36:37], v[24:25], s[10:11], v[74:75] op_sel_hi:[1,0,1]
	v_pk_fma_f32 v[34:35], v[22:23], s[10:11], v[90:91] op_sel_hi:[1,0,1]
	v_lshlrev_b32_e32 v22, 16, v32
	v_and_b32_e32 v23, 0xffff0000, v32
	v_lshlrev_b32_e32 v24, 16, v33
	v_and_b32_e32 v25, 0xffff0000, v33
	v_pk_fma_f32 v[30:31], v[24:25], s[10:11], v[80:81] op_sel_hi:[1,0,1]
	v_pk_fma_f32 v[32:33], v[22:23], s[10:11], v[82:83] op_sel_hi:[1,0,1]
	v_lshlrev_b32_e32 v22, 16, v70
	v_and_b32_e32 v23, 0xffff0000, v70
	v_lshlrev_b32_e32 v24, 16, v71
	v_and_b32_e32 v25, 0xffff0000, v71
	v_pk_fma_f32 v[24:25], v[24:25], s[10:11], v[94:95] op_sel_hi:[1,0,1]
	v_pk_fma_f32 v[28:29], v[22:23], s[10:11], v[88:89] op_sel_hi:[1,0,1]
	v_add_f32_e32 v74, v34, v35
	v_add_f32_e32 v80, v36, v37
	v_and_b32_e32 v27, 0xffff0000, v72
	v_lshlrev_b32_e32 v22, 16, v73
	v_and_b32_e32 v23, 0xffff0000, v73
	v_mov_b32_e32 v70, v32
	v_mov_b32_e32 v71, v28
	v_mov_b32_e32 v72, v33
	v_mov_b32_e32 v73, v29
	v_mov_b32_e32 v75, v24
	v_mov_b32_e32 v81, v25
	v_pk_fma_f32 v[26:27], v[26:27], s[10:11], v[96:97] op_sel_hi:[1,0,1]
	v_pk_add_f32 v[70:71], v[70:71], v[72:73]
	v_pk_add_f32 v[72:73], v[74:75], v[80:81]
	v_pk_fma_f32 v[22:23], v[22:23], s[10:11], v[86:87] op_sel_hi:[1,0,1]
	v_pk_add_f32 v[70:71], v[70:71], v[72:73]
	v_mov_b32_e32 v72, v30
	v_mov_b32_e32 v73, v26
	v_mov_b32_e32 v74, v31
	v_mov_b32_e32 v75, v27
	v_pk_add_f32 v[72:73], v[72:73], v[74:75]
	v_mov_b32_e32 v79, v22
	v_mov_b32_e32 v77, v23
	v_pk_add_f32 v[70:71], v[72:73], v[70:71]
	v_pk_add_f32 v[72:73], v[78:79], v[76:77]
	s_nop 0
	v_pk_add_f32 v[70:71], v[72:73], v[70:71]
	s_nop 0
	v_add_f32_e32 v69, v70, v71
	v_cndmask_b32_e32 v70, v58, v61, vcc
	v_lshlrev_b32_e32 v102, 2, v70
	ds_bpermute_b32 v70, v102, v69
	v_cmp_lt_i32_e32 vcc, v62, v60
	s_waitcnt lgkmcnt(0)
	v_add_f32_e32 v69, v69, v70
	v_cndmask_b32_e32 v70, v58, v62, vcc
	v_lshlrev_b32_e32 v103, 2, v70
	ds_bpermute_b32 v70, v103, v69
	v_cmp_lt_i32_e32 vcc, v63, v60
	s_waitcnt lgkmcnt(0)
	v_add_f32_e32 v69, v69, v70
	v_cndmask_b32_e32 v70, v58, v63, vcc
	v_lshlrev_b32_e32 v104, 2, v70
	ds_bpermute_b32 v70, v104, v69
	v_cmp_lt_i32_e32 vcc, v64, v60
	s_waitcnt lgkmcnt(0)
	v_add_f32_e32 v69, v69, v70
	v_cndmask_b32_e32 v70, v58, v64, vcc
	v_lshlrev_b32_e32 v105, 2, v70
	ds_bpermute_b32 v70, v105, v69
	v_cmp_lt_i32_e32 vcc, v65, v60
	s_waitcnt lgkmcnt(0)
	v_add_f32_e32 v69, v69, v70
	v_cndmask_b32_e32 v70, v58, v65, vcc
	v_lshlrev_b32_e32 v106, 2, v70
	ds_bpermute_b32 v70, v106, v69
	v_cmp_lt_i32_e32 vcc, v66, v60
	s_waitcnt lgkmcnt(0)
	v_add_f32_e32 v69, v69, v70
	v_cndmask_b32_e32 v70, v58, v66, vcc
	v_lshlrev_b32_e32 v107, 2, v70
	ds_bpermute_b32 v70, v107, v69
	s_waitcnt lgkmcnt(0)
	v_add_f32_e32 v69, v69, v70
	v_fmamk_f32 v53, v69, 0xba000000, v53
	v_fmac_f32_e32 v52, 0xba000000, v69
	v_fmamk_f32 v51, v69, 0xba000000, v51
	v_fmac_f32_e32 v50, 0xba000000, v69
	v_pk_mul_f32 v[70:71], v[50:51], v[50:51]
	v_pk_mul_f32 v[72:73], v[52:53], v[52:53]
	v_fmamk_f32 v49, v69, 0xba000000, v49
	v_fmac_f32_e32 v48, 0xba000000, v69
	v_fmamk_f32 v47, v69, 0xba000000, v47
	v_fmac_f32_e32 v46, 0xba000000, v69
	v_pk_mov_b32 v[74:75], v[72:73], v[70:71] op_sel:[1,0]
	v_mov_b32_e32 v73, v71
	v_pk_add_f32 v[70:71], v[74:75], v[72:73]
	v_pk_mul_f32 v[72:73], v[46:47], v[46:47]
	v_pk_mul_f32 v[74:75], v[48:49], v[48:49]
	v_mov_b32_e32 v76, v72
	v_mov_b32_e32 v77, v74
	v_mov_b32_e32 v74, v73
	v_pk_add_f32 v[70:71], v[70:71], v[70:71] op_sel:[0,1] op_sel_hi:[1,0]
	v_pk_add_f32 v[72:73], v[76:77], v[74:75]
	v_fmamk_f32 v43, v69, 0xba000000, v43
	v_pk_add_f32 v[70:71], v[72:73], v[70:71] op_sel:[1,0] op_sel_hi:[0,1]
	v_fmac_f32_e32 v42, 0xba000000, v69
	v_fmamk_f32 v45, v69, 0xba000000, v45
	v_fmac_f32_e32 v44, 0xba000000, v69
	v_pk_add_f32 v[86:87], v[72:73], v[70:71]
	v_pk_mul_f32 v[70:71], v[44:45], v[44:45]
	v_pk_mul_f32 v[72:73], v[42:43], v[42:43]
	v_fmamk_f32 v39, v69, 0xba000000, v39
	v_fmac_f32_e32 v38, 0xba000000, v69
	v_fmamk_f32 v41, v69, 0xba000000, v41
	v_fmac_f32_e32 v40, 0xba000000, v69
	v_pk_mov_b32 v[74:75], v[72:73], v[70:71] op_sel:[1,0]
	v_mov_b32_e32 v73, v71
	v_pk_add_f32 v[70:71], v[74:75], v[72:73]
	v_pk_mul_f32 v[72:73], v[40:41], v[40:41]
	v_pk_mul_f32 v[74:75], v[38:39], v[38:39]
	v_mov_b32_e32 v76, v72
	v_mov_b32_e32 v77, v74
	v_mov_b32_e32 v74, v73
	v_pk_add_f32 v[70:71], v[70:71], v[70:71] op_sel:[0,1] op_sel_hi:[1,0]
	v_pk_add_f32 v[72:73], v[76:77], v[74:75]
	v_fmac_f32_e32 v34, 0xba000000, v69
	v_pk_add_f32 v[70:71], v[72:73], v[70:71] op_sel:[1,0] op_sel_hi:[0,1]
	v_pk_add_f32 v[88:89], v[72:73], v[70:71]
	v_fmamk_f32 v35, v69, 0xba000000, v35
	v_fmac_f32_e32 v36, 0xba000000, v69
	v_mul_f32_e32 v70, v34, v34
	v_fmamk_f32 v37, v69, 0xba000000, v37
	v_pk_fma_f32 v[90:91], v[34:35], v[34:35], v[70:71] op_sel_hi:[1,1,0]
	v_mul_f32_e32 v70, v36, v36
	v_pk_fma_f32 v[92:93], v[36:37], v[36:37], v[70:71] op_sel_hi:[1,1,0]
	v_fmamk_f32 v33, v69, 0xba000000, v33
	v_fmamk_f32 v29, v69, 0xba000000, v29
	v_fmac_f32_e32 v32, 0xba000000, v69
	v_fmac_f32_e32 v28, 0xba000000, v69
	v_fmamk_f32 v25, v69, 0xba000000, v25
	v_fmac_f32_e32 v24, 0xba000000, v69
	v_mov_b32_e32 v100, v29
	v_mov_b32_e32 v101, v33
	v_mul_f32_e32 v90, v24, v24
	v_mul_f32_e32 v92, v25, v25
	v_mov_b32_e32 v98, v28
	v_mov_b32_e32 v99, v32
	v_pk_mul_f32 v[100:101], v[100:101], v[100:101]
	v_fmamk_f32 v31, v69, 0xba000000, v31
	v_fmamk_f32 v27, v69, 0xba000000, v27
	v_pk_fma_f32 v[98:99], v[98:99], v[98:99], v[100:101]
	v_pk_add_f32 v[90:91], v[90:91], v[92:93]
	v_fmac_f32_e32 v30, 0xba000000, v69
	v_fmac_f32_e32 v26, 0xba000000, v69
	v_pk_add_f32 v[90:91], v[98:99], v[90:91]
	v_mov_b32_e32 v98, v27
	v_mov_b32_e32 v99, v31
	v_fmamk_f32 v23, v69, 0xba000000, v23
	v_fmac_f32_e32 v22, 0xba000000, v69
	v_mov_b32_e32 v92, v26
	v_mov_b32_e32 v93, v30
	v_pk_mul_f32 v[98:99], v[98:99], v[98:99]
	v_mul_f32_e32 v94, v22, v22
	v_mul_f32_e32 v96, v23, v23
	v_pk_fma_f32 v[92:93], v[92:93], v[92:93], v[98:99]
	v_mov_b32_e32 v95, v86
	v_mov_b32_e32 v97, v88
	v_pk_add_f32 v[90:91], v[92:93], v[90:91]
	v_pk_add_f32 v[86:87], v[94:95], v[96:97]
	s_nop 0
	v_pk_add_f32 v[86:87], v[90:91], v[86:87]
	s_nop 0
	v_add_f32_e32 v69, v86, v87
	ds_bpermute_b32 v86, v102, v69
	s_waitcnt lgkmcnt(0)
; #define GAS __attribute__((address_space(1)))
; template <bool Y8, bool LAST>
; __device__ __forceinline__ void combine_ln2_phase(Frame& F, int layer) {
;     ...
;         const float rstd = rsqrtf(wave_sum(s2) * (1.0f / D_MODEL) + LN_EPS);
; #pragma unroll
;         for (int j = 0; j < 4; ++j) { const int c = 8 * lane + 512 * j;
;             const f32x4 o0 = a[j][0] * rstd * *(const GAS f32x4*)(g2 + c) + *(const GAS f32x4*)(b2 + c), o1 = a[j][1] * rstd * *(const GAS f32x4*)(g2 + c + 4) + *(const GAS f32x4*)(b2 + c + 4);
;             if constexpr (LAST) { *(GAS f32x4*)(OUT + (size_t)t * D_MODEL + c) = o0; *(GAS f32x4*)(OUT + (size_t)t * D_MODEL + c + 4) = o1; }
	v_add_f32_e32 v69, v69, v86
	ds_bpermute_b32 v86, v103, v69
	s_waitcnt lgkmcnt(0)
	v_add_f32_e32 v69, v69, v86
	ds_bpermute_b32 v86, v104, v69
	s_waitcnt lgkmcnt(0)
	v_add_f32_e32 v69, v69, v86
	ds_bpermute_b32 v86, v105, v69
	s_waitcnt lgkmcnt(0)
	v_add_f32_e32 v69, v69, v86
	ds_bpermute_b32 v86, v106, v69
	s_waitcnt lgkmcnt(0)
	v_add_f32_e32 v69, v69, v86
	ds_bpermute_b32 v86, v107, v69
	s_waitcnt lgkmcnt(0)
	v_add_f32_e32 v69, v69, v86
	v_fmamk_f32 v69, v69, 0x3a000000, v54
	v_mul_f32_e32 v86, 0x4b800000, v69
	v_cmp_gt_f32_e32 vcc, s21, v69
	s_nop 1
	v_cndmask_b32_e32 v69, v69, v86, vcc
	v_rsq_f32_e32 v69, v69
	s_nop 0
	v_mul_f32_e32 v86, 0x45800000, v69
	v_cndmask_b32_e32 v86, v69, v86, vcc
	v_pk_mul_f32 v[88:89], v[52:53], v[86:87] op_sel_hi:[1,0]
	v_pk_mul_f32 v[50:51], v[50:51], v[86:87] op_sel_hi:[1,0]
	v_pk_mul_f32 v[46:47], v[46:47], v[86:87] op_sel_hi:[1,0]
	v_pk_fma_f32 v[52:53], v[134:135], v[50:51], v[142:143]
	v_pk_fma_f32 v[50:51], v[132:133], v[88:89], v[140:141]
	v_pk_mul_f32 v[74:75], v[48:49], v[86:87] op_sel_hi:[1,0]
	v_pk_fma_f32 v[48:49], v[130:131], v[46:47], v[138:139]
	v_pk_fma_f32 v[46:47], v[128:129], v[74:75], v[136:137]
	global_store_dwordx4 v55, v[50:53], s[14:15]
	global_store_dwordx4 v55, v[46:49], s[14:15] offset:16
	s_nop 0
	v_pk_mul_f32 v[44:45], v[44:45], v[86:87] op_sel_hi:[1,0]
	v_pk_mul_f32 v[42:43], v[42:43], v[86:87] op_sel_hi:[1,0]
	v_pk_mul_f32 v[40:41], v[40:41], v[86:87] op_sel_hi:[1,0]
	v_pk_mul_f32 v[38:39], v[38:39], v[86:87] op_sel_hi:[1,0]
	v_pk_mul_f32 v[36:37], v[36:37], v[86:87] op_sel_hi:[1,0]
	v_pk_mul_f32 v[34:35], v[34:35], v[86:87] op_sel_hi:[1,0]
	v_pk_mul_f32 v[24:25], v[24:25], v[86:87] op_sel_hi:[1,0]
	v_pk_mul_f32 v[28:29], v[28:29], v[86:87] op_sel_hi:[1,0]
	v_pk_fma_f32 v[42:43], v[148:149], v[42:43], v[144:145]
	v_pk_fma_f32 v[44:45], v[150:151], v[44:45], v[146:147]
	v_pk_fma_f32 v[38:39], v[152:153], v[38:39], v[156:157]
	v_pk_fma_f32 v[40:41], v[154:155], v[40:41], v[158:159]
	global_store_dwordx4 v55, v[42:45], s[14:15] offset:2048
	global_store_dwordx4 v55, v[38:41], s[14:15] offset:2064
	s_nop 0
	v_pk_fma_f32 v[34:35], v[164:165], v[34:35], v[160:161]
	v_pk_fma_f32 v[36:37], v[166:167], v[36:37], v[162:163]
	v_pk_mul_f32 v[38:39], v[30:31], v[86:87] op_sel_hi:[1,0]
	v_pk_mul_f32 v[30:31], v[32:33], v[86:87] op_sel_hi:[1,0]
	v_pk_fma_f32 v[32:33], v[170:171], v[38:39], v[174:175]
	v_pk_fma_f32 v[30:31], v[168:169], v[30:31], v[172:173]
	global_store_dwordx4 v56, v[34:37], s[14:15]
	global_store_dwordx4 v56, v[30:33], s[14:15] offset:16
	s_nop 0
	v_pk_fma_f32 v[28:29], v[180:181], v[28:29], v[176:177]
	v_pk_fma_f32 v[30:31], v[182:183], v[24:25], v[178:179]
	v_pk_mul_f32 v[24:25], v[22:23], v[86:87] op_sel_hi:[1,0]
	v_pk_mul_f32 v[22:23], v[26:27], v[86:87] op_sel_hi:[1,0]
	v_pk_fma_f32 v[24:25], v[186:187], v[24:25], v[190:191]
	v_pk_fma_f32 v[22:23], v[184:185], v[22:23], v[188:189]
	global_store_dwordx4 v57, v[28:31], s[14:15]
	global_store_dwordx4 v57, v[22:25], s[14:15] offset:16
	s_cselect_b64 s[14:15], -1, 0
	s_branch .LBB0_3261
